# P11 routing: per-lane top-16 of 64 keys by 16-key odd-even merge sorts + bitonic top-16 merges (924 instructions) instead of 64 serial 16-slot insertions (2528)
# baseline (speedup 1.0000x reference)
; __device__ __forceinline__ void p11_route(Frame& F) {
;     ...
;     for (int item = F.gw; item < (S_ / 16) * PH; item += F.NGW) {
;         const int tile = item >> 3, h = item & 7, t0 = tile * 16;
; #pragma unroll
;         for (int c = 0; c < 2; ++c) {
;             f32x4 acc[8];
; #pragma unroll
;             for (int nt = 0; nt < 8; ++nt) acc[nt] = (f32x4){0.f, 0.f, 0.f, 0.f};
; #pragma unroll
;             for (int ks = 0; ks < 4; ++ks) { const gbf16x8 a = *(const gbf16x8*)(QRY + (size_t)(t0 + l15) * 2048 + h * 256 + c * 128 + 32 * ks + 8 * g);
; #pragma unroll
;                 for (int nt = 0; nt < 8; ++nt) acc[nt] = __builtin_amdgcn_mfma_f32_16x16x32_bf16(a, *(const gbf16x8*)(SK + ((size_t)(h * 2 + c) * PNK + 16 * nt + l15) * 128 + 32 * ks + 8 * g), acc[nt], 0, 0, 0); }
.LBB0_3214:
	s_lshl_b32 s4, s17, 1
	s_and_b32 s18, s4, -16
	s_waitcnt lgkmcnt(0)
	v_or_b32_e32 v126, s18, v150
	v_ashrrev_i32_e32 v127, 31, v126
	v_lshlrev_b64 v[126:127], 12, v[126:127]
	v_lshl_add_u64 v[126:127], v[2:3], 0, v[126:127]
	global_load_dwordx4 v[128:131], v[126:127], off
	global_load_dwordx4 v[132:135], v[4:5], off
	global_load_dwordx4 v[136:139], v[6:7], off
	global_load_dwordx4 v[140:143], v[8:9], off
	global_load_dwordx4 v[144:147], v[10:11], off
	global_load_dwordx4 v[160:163], v[12:13], off
	global_load_dwordx4 v[164:167], v[14:15], off
	global_load_dwordx4 v[168:171], v[16:17], off
	global_load_dwordx4 v[172:175], v[18:19], off
	global_load_dwordx4 v[176:179], v[126:127], off offset:64
	global_load_dwordx4 v[180:183], v[4:5], off offset:64
	global_load_dwordx4 v[184:187], v[20:21], off
	global_load_dwordx4 v[188:191], v[22:23], off
	global_load_dwordx4 v[192:195], v[24:25], off
	global_load_dwordx4 v[196:199], v[26:27], off
	global_load_dwordx4 v[200:203], v[28:29], off
	global_load_dwordx4 v[204:207], v[30:31], off
	global_load_dwordx4 v[208:211], v[32:33], off
	global_load_dwordx4 v[212:215], v[126:127], off offset:128
	global_load_dwordx4 v[216:219], v[4:5], off offset:128
	global_load_dwordx4 v[220:223], v[34:35], off
	global_load_dwordx4 v[224:227], v[36:37], off
	global_load_dwordx4 v[228:231], v[38:39], off
	global_load_dwordx4 v[232:235], v[40:41], off
	global_load_dwordx4 v[236:239], v[42:43], off
	global_load_dwordx4 v[240:243], v[44:45], off
	global_load_dwordx4 v[244:247], v[46:47], off
	s_mov_b32 s4, 0
	v_mov_b32_e32 v148, 0xff800000
	v_mov_b32_e32 v149, 0xff800000
	v_mov_b32_e32 v159, 0xff800000
	s_waitcnt vmcnt(25)
	v_mfma_f32_16x16x32_bf16 v[132:135], v[128:131], v[132:135], 0
	s_waitcnt vmcnt(24)
	v_mfma_f32_16x16x32_bf16 v[136:139], v[128:131], v[136:139], 0
	s_waitcnt vmcnt(23)
	v_mfma_f32_16x16x32_bf16 v[140:143], v[128:131], v[140:143], 0
	s_waitcnt vmcnt(22)
	v_mfma_f32_16x16x32_bf16 v[144:147], v[128:131], v[144:147], 0
	s_waitcnt vmcnt(21)
	v_mfma_f32_16x16x32_bf16 v[160:163], v[128:131], v[160:163], 0
	s_waitcnt vmcnt(20)
	v_mfma_f32_16x16x32_bf16 v[164:167], v[128:131], v[164:167], 0
	s_waitcnt vmcnt(19)
	v_mfma_f32_16x16x32_bf16 v[168:171], v[128:131], v[168:171], 0
	s_waitcnt vmcnt(18)
	v_mfma_f32_16x16x32_bf16 v[128:131], v[128:131], v[172:175], 0
	s_waitcnt vmcnt(16)
	v_mfma_f32_16x16x32_bf16 v[132:135], v[176:179], v[180:183], v[132:135]
	s_waitcnt vmcnt(15)
	v_mfma_f32_16x16x32_bf16 v[136:139], v[176:179], v[184:187], v[136:139]
	s_waitcnt vmcnt(14)
	v_mfma_f32_16x16x32_bf16 v[140:143], v[176:179], v[188:191], v[140:143]
	s_waitcnt vmcnt(13)
	v_mfma_f32_16x16x32_bf16 v[144:147], v[176:179], v[192:195], v[144:147]
	s_waitcnt vmcnt(12)
	v_mfma_f32_16x16x32_bf16 v[160:163], v[176:179], v[196:199], v[160:163]
	s_waitcnt vmcnt(11)
	v_mfma_f32_16x16x32_bf16 v[164:167], v[176:179], v[200:203], v[164:167]
	s_waitcnt vmcnt(10)
	v_mfma_f32_16x16x32_bf16 v[168:171], v[176:179], v[204:207], v[168:171]
	s_waitcnt vmcnt(9)
	v_mfma_f32_16x16x32_bf16 v[128:131], v[176:179], v[208:211], v[128:131]
	global_load_dwordx4 v[176:179], v[126:127], off offset:192
	global_load_dwordx4 v[180:183], v[4:5], off offset:192
	global_load_dwordx4 v[184:187], v[48:49], off
	global_load_dwordx4 v[188:191], v[50:51], off
	global_load_dwordx4 v[192:195], v[52:53], off
	global_load_dwordx4 v[196:199], v[54:55], off
	global_load_dwordx4 v[200:203], v[56:57], off
	global_load_dwordx4 v[204:207], v[58:59], off
	global_load_dwordx4 v[208:211], v[60:61], off
	s_waitcnt vmcnt(16)
	v_mfma_f32_16x16x32_bf16 v[132:135], v[212:215], v[216:219], v[132:135]
	s_waitcnt vmcnt(15)
	v_mfma_f32_16x16x32_bf16 v[136:139], v[212:215], v[220:223], v[136:139]
	s_waitcnt vmcnt(14)
	v_mfma_f32_16x16x32_bf16 v[140:143], v[212:215], v[224:227], v[140:143]
	s_waitcnt vmcnt(13)
	v_mfma_f32_16x16x32_bf16 v[144:147], v[212:215], v[228:231], v[144:147]
	s_waitcnt vmcnt(12)
	v_mfma_f32_16x16x32_bf16 v[160:163], v[212:215], v[232:235], v[160:163]
	s_waitcnt vmcnt(11)
	v_mfma_f32_16x16x32_bf16 v[164:167], v[212:215], v[236:239], v[164:167]
	s_waitcnt vmcnt(10)
	v_mfma_f32_16x16x32_bf16 v[168:171], v[212:215], v[240:243], v[168:171]
	s_waitcnt vmcnt(9)
	v_mfma_f32_16x16x32_bf16 v[128:131], v[212:215], v[244:247], v[128:131]
	s_waitcnt vmcnt(7)
	v_mfma_f32_16x16x32_bf16 v[132:135], v[176:179], v[180:183], v[132:135]
	s_waitcnt vmcnt(6)
	v_mfma_f32_16x16x32_bf16 v[136:139], v[176:179], v[184:187], v[136:139]
	s_waitcnt vmcnt(5)
	v_mfma_f32_16x16x32_bf16 v[140:143], v[176:179], v[188:191], v[140:143]
	s_waitcnt vmcnt(4)
	v_mfma_f32_16x16x32_bf16 v[144:147], v[176:179], v[192:195], v[144:147]
	s_waitcnt vmcnt(3)
	v_mfma_f32_16x16x32_bf16 v[160:163], v[176:179], v[196:199], v[160:163]
	s_waitcnt vmcnt(2)
	v_mfma_f32_16x16x32_bf16 v[164:167], v[176:179], v[200:203], v[164:167]
	s_waitcnt vmcnt(1)
	v_mfma_f32_16x16x32_bf16 v[168:171], v[176:179], v[204:207], v[168:171]
	s_waitcnt vmcnt(0)
; __device__ __forceinline__ void p11_route(Frame& F) {
;     ...
;             for (int ks = 0; ks < 4; ++ks) { const gbf16x8 a = *(const gbf16x8*)(QRY + (size_t)(t0 + l15) * 2048 + h * 256 + c * 128 + 32 * ks + 8 * g);
; #pragma unroll
;                 for (int nt = 0; nt < 8; ++nt) acc[nt] = __builtin_amdgcn_mfma_f32_16x16x32_bf16(a, *(const gbf16x8*)(SK + ((size_t)(h * 2 + c) * PNK + 16 * nt + l15) * 128 + 32 * ks + 8 * g), acc[nt], 0, 0, 0); }
; #pragma unroll
;             for (int nt = 0; nt < 8; ++nt)
; #pragma unroll
;                 for (int r = 0; r < 4; ++r) sc[(c * 16 + 4 * g + r) * 129 + 16 * nt + l15] = acc[nt][r];
	v_mfma_f32_16x16x32_bf16 v[128:131], v[176:179], v[208:211], v[128:131]
	s_nop 3
	ds_write2_b32 v151, v132, v136 offset1:16
	ds_write2_b32 v151, v133, v137 offset0:129 offset1:145
	v_add_u32_e32 v132, 0x400, v151
	ds_write2_b32 v132, v134, v138 offset0:2 offset1:18
	ds_write2_b32 v132, v135, v139 offset0:131 offset1:147
	ds_write2_b32 v151, v140, v144 offset0:32 offset1:48
	ds_write2_b32 v151, v141, v145 offset0:161 offset1:177
	ds_write2_b32 v132, v142, v146 offset0:34 offset1:50
	ds_write2_b32 v132, v143, v147 offset0:163 offset1:179
	ds_write2_b32 v151, v160, v164 offset0:64 offset1:80
	ds_write2_b32 v151, v161, v165 offset0:193 offset1:209
	ds_write2_b32 v132, v162, v166 offset0:66 offset1:82
	ds_write2_b32 v132, v163, v167 offset0:195 offset1:211
	ds_write2_b32 v151, v168, v128 offset0:96 offset1:112
	ds_write2_b32 v151, v169, v129 offset0:225 offset1:241
	ds_write2_b32 v132, v170, v130 offset0:98 offset1:114
	ds_write2_b32 v132, v171, v131 offset0:227 offset1:243
	global_load_dwordx4 v[128:131], v[126:127], off offset:256
	global_load_dwordx4 v[132:135], v[62:63], off
	global_load_dwordx4 v[136:139], v[64:65], off
	global_load_dwordx4 v[140:143], v[66:67], off
	global_load_dwordx4 v[144:147], v[68:69], off
	global_load_dwordx4 v[160:163], v[70:71], off
	global_load_dwordx4 v[164:167], v[72:73], off
	global_load_dwordx4 v[168:171], v[74:75], off
	global_load_dwordx4 v[172:175], v[76:77], off
	global_load_dwordx4 v[176:179], v[126:127], off offset:320
	global_load_dwordx4 v[180:183], v[78:79], off
	global_load_dwordx4 v[184:187], v[80:81], off
	global_load_dwordx4 v[188:191], v[82:83], off
	global_load_dwordx4 v[192:195], v[84:85], off
	global_load_dwordx4 v[196:199], v[86:87], off
	global_load_dwordx4 v[200:203], v[88:89], off
	global_load_dwordx4 v[204:207], v[90:91], off
	global_load_dwordx4 v[208:211], v[92:93], off
	global_load_dwordx4 v[212:215], v[126:127], off offset:384
	global_load_dwordx4 v[216:219], v[94:95], off
	global_load_dwordx4 v[220:223], v[96:97], off
	global_load_dwordx4 v[224:227], v[98:99], off
	global_load_dwordx4 v[228:231], v[100:101], off
	global_load_dwordx4 v[232:235], v[102:103], off
	global_load_dwordx4 v[236:239], v[104:105], off
	global_load_dwordx4 v[240:243], v[106:107], off
	global_load_dwordx4 v[244:247], v[108:109], off
	s_waitcnt vmcnt(25)
	v_mfma_f32_16x16x32_bf16 v[132:135], v[128:131], v[132:135], 0
	s_waitcnt vmcnt(24)
	v_mfma_f32_16x16x32_bf16 v[136:139], v[128:131], v[136:139], 0
	s_waitcnt vmcnt(23)
	v_mfma_f32_16x16x32_bf16 v[140:143], v[128:131], v[140:143], 0
	s_waitcnt vmcnt(22)
	v_mfma_f32_16x16x32_bf16 v[144:147], v[128:131], v[144:147], 0
	s_waitcnt vmcnt(21)
	v_mfma_f32_16x16x32_bf16 v[160:163], v[128:131], v[160:163], 0
	s_waitcnt vmcnt(20)
	v_mfma_f32_16x16x32_bf16 v[164:167], v[128:131], v[164:167], 0
	s_waitcnt vmcnt(19)
	v_mfma_f32_16x16x32_bf16 v[168:171], v[128:131], v[168:171], 0
	s_waitcnt vmcnt(18)
	v_mfma_f32_16x16x32_bf16 v[128:131], v[128:131], v[172:175], 0
	s_waitcnt vmcnt(16)
	v_mfma_f32_16x16x32_bf16 v[132:135], v[176:179], v[180:183], v[132:135]
	s_waitcnt vmcnt(15)
	v_mfma_f32_16x16x32_bf16 v[136:139], v[176:179], v[184:187], v[136:139]
	s_waitcnt vmcnt(14)
	v_mfma_f32_16x16x32_bf16 v[140:143], v[176:179], v[188:191], v[140:143]
	s_waitcnt vmcnt(13)
	v_mfma_f32_16x16x32_bf16 v[144:147], v[176:179], v[192:195], v[144:147]
	s_waitcnt vmcnt(12)
	v_mfma_f32_16x16x32_bf16 v[160:163], v[176:179], v[196:199], v[160:163]
	s_waitcnt vmcnt(11)
	v_mfma_f32_16x16x32_bf16 v[164:167], v[176:179], v[200:203], v[164:167]
	s_waitcnt vmcnt(10)
	v_mfma_f32_16x16x32_bf16 v[168:171], v[176:179], v[204:207], v[168:171]
	s_waitcnt vmcnt(9)
	v_mfma_f32_16x16x32_bf16 v[128:131], v[176:179], v[208:211], v[128:131]
	global_load_dwordx4 v[176:179], v[126:127], off offset:448
	global_load_dwordx4 v[180:183], v[110:111], off
	global_load_dwordx4 v[184:187], v[112:113], off
	global_load_dwordx4 v[188:191], v[114:115], off
	global_load_dwordx4 v[192:195], v[116:117], off
	global_load_dwordx4 v[196:199], v[118:119], off
	global_load_dwordx4 v[200:203], v[120:121], off
	global_load_dwordx4 v[204:207], v[122:123], off
	global_load_dwordx4 v[208:211], v[124:125], off
	s_waitcnt vmcnt(16)
	v_mfma_f32_16x16x32_bf16 v[132:135], v[212:215], v[216:219], v[132:135]
	s_waitcnt vmcnt(15)
	v_mfma_f32_16x16x32_bf16 v[136:139], v[212:215], v[220:223], v[136:139]
	s_waitcnt vmcnt(14)
	v_mfma_f32_16x16x32_bf16 v[140:143], v[212:215], v[224:227], v[140:143]
	s_waitcnt vmcnt(13)
	v_mfma_f32_16x16x32_bf16 v[144:147], v[212:215], v[228:231], v[144:147]
	s_waitcnt vmcnt(12)
	v_mfma_f32_16x16x32_bf16 v[160:163], v[212:215], v[232:235], v[160:163]
	s_waitcnt vmcnt(11)
	v_mfma_f32_16x16x32_bf16 v[164:167], v[212:215], v[236:239], v[164:167]
	s_waitcnt vmcnt(10)
	v_mfma_f32_16x16x32_bf16 v[168:171], v[212:215], v[240:243], v[168:171]
	s_waitcnt vmcnt(9)
	v_mfma_f32_16x16x32_bf16 v[128:131], v[212:215], v[244:247], v[128:131]
	s_waitcnt vmcnt(7)
	v_mfma_f32_16x16x32_bf16 v[132:135], v[176:179], v[180:183], v[132:135]
	s_waitcnt vmcnt(6)
	v_mfma_f32_16x16x32_bf16 v[136:139], v[176:179], v[184:187], v[136:139]
	s_waitcnt vmcnt(5)
	v_mfma_f32_16x16x32_bf16 v[140:143], v[176:179], v[188:191], v[140:143]
	s_waitcnt vmcnt(4)
	v_mfma_f32_16x16x32_bf16 v[144:147], v[176:179], v[192:195], v[144:147]
	s_waitcnt vmcnt(3)
	v_mfma_f32_16x16x32_bf16 v[160:163], v[176:179], v[196:199], v[160:163]
	s_waitcnt vmcnt(2)
	v_mfma_f32_16x16x32_bf16 v[164:167], v[176:179], v[200:203], v[164:167]
	s_waitcnt vmcnt(1)
	v_mfma_f32_16x16x32_bf16 v[168:171], v[176:179], v[204:207], v[168:171]
	s_waitcnt vmcnt(0)
; #define LAS __attribute__((address_space(3)))
; #define INS16(A_, X_) do { float x_ = (X_); _Pragma("unroll") for (int i_ = 0; i_ < 16; ++i_) { const float hi_ = fmaxf(A_[i_], x_); x_ = fminf(A_[i_], x_); A_[i_] = hi_; } } while (0)
; __device__ __forceinline__ float uniq_key(float s, int n) { return __uint_as_float((__float_as_uint(s) & ~0xffu) | (unsigned)(255 - n)); }
; __device__ __forceinline__ void p11_route(Frame& F) {
;     ...
;         { LAS float* row = sc + (F.lane & 31) * 129; float a[16]; const int nb = (F.lane >> 5) * (PNK / 2);
; #pragma unroll
;             for (int i = 0; i < 16; ++i) a[i] = -INFINITY;
; #pragma unroll 4
;             for (int n = 0; n < PNK / 2; ++n) INS16(a, uniq_key(row[nb + n], nb + n));
	v_mfma_f32_16x16x32_bf16 v[126:129], v[176:179], v[208:211], v[128:131]
	s_nop 2
	v_add_u32_e32 v130, 0x2000, v151
	v_add_u32_e32 v131, 0x2400, v151
	ds_write2_b32 v130, v132, v136 offset0:16 offset1:32
	ds_write2_b32 v130, v133, v137 offset0:145 offset1:161
	ds_write2_b32 v131, v134, v138 offset0:18 offset1:34
	ds_write2_b32 v131, v135, v139 offset0:147 offset1:163
	ds_write2_b32 v130, v140, v144 offset0:48 offset1:64
	ds_write2_b32 v130, v141, v145 offset0:177 offset1:193
	ds_write2_b32 v131, v142, v146 offset0:50 offset1:66
	ds_write2_b32 v131, v143, v147 offset0:179 offset1:195
	ds_write2_b32 v130, v160, v164 offset0:80 offset1:96
	ds_write2_b32 v130, v161, v165 offset0:209 offset1:225
	ds_write2_b32 v131, v162, v166 offset0:82 offset1:98
	ds_write2_b32 v131, v163, v167 offset0:211 offset1:227
	ds_write2_b32 v130, v168, v126 offset0:112 offset1:128
	v_add_u32_e32 v126, 0x2200, v151
	ds_write2_b32 v126, v169, v127 offset0:113 offset1:129
	ds_write2_b32 v131, v170, v128 offset0:114 offset1:130
	v_add_u32_e32 v126, 0x2600, v151
	ds_write2_b32 v126, v171, v129 offset0:115 offset1:131
	ds_read2_b32 v[222:223], v155 offset0:0 offset1:1
	ds_read2_b32 v[224:225], v155 offset0:2 offset1:3
	ds_read2_b32 v[226:227], v155 offset0:4 offset1:5
	ds_read2_b32 v[228:229], v155 offset0:6 offset1:7
	ds_read2_b32 v[230:231], v155 offset0:8 offset1:9
	ds_read2_b32 v[232:233], v155 offset0:10 offset1:11
	ds_read2_b32 v[234:235], v155 offset0:12 offset1:13
	ds_read2_b32 v[236:237], v155 offset0:14 offset1:15
	s_waitcnt lgkmcnt(0)
	ds_read2_b32 v[238:239], v155 offset0:16 offset1:17
	ds_read2_b32 v[240:241], v155 offset0:18 offset1:19
	ds_read2_b32 v[242:243], v155 offset0:20 offset1:21
	ds_read2_b32 v[244:245], v155 offset0:22 offset1:23
	ds_read2_b32 v[246:247], v155 offset0:24 offset1:25
	ds_read2_b32 v[248:249], v155 offset0:26 offset1:27
	ds_read2_b32 v[250:251], v155 offset0:28 offset1:29
	ds_read2_b32 v[252:253], v155 offset0:30 offset1:31
	v_add_u32_e32 v127, 3, v156
	v_and_or_b32 v222, v222, s14, v127
	v_add_u32_e32 v130, 2, v156
	v_and_or_b32 v223, v223, s14, v130
	v_add_u32_e32 v127, 1, v156
	v_and_or_b32 v224, v224, s14, v127
	v_add_u32_e32 v130, 0, v156
	v_and_or_b32 v225, v225, s14, v130
	v_add_u32_e32 v127, -1, v156
	v_and_or_b32 v226, v226, s14, v127
	v_add_u32_e32 v130, -2, v156
	v_and_or_b32 v227, v227, s14, v130
	v_add_u32_e32 v127, -3, v156
	v_and_or_b32 v228, v228, s14, v127
	v_add_u32_e32 v130, -4, v156
	v_and_or_b32 v229, v229, s14, v130
	v_add_u32_e32 v127, -5, v156
	v_and_or_b32 v230, v230, s14, v127
	v_add_u32_e32 v130, -6, v156
	v_and_or_b32 v231, v231, s14, v130
	v_add_u32_e32 v127, -7, v156
	v_and_or_b32 v232, v232, s14, v127
	v_add_u32_e32 v130, -8, v156
	v_and_or_b32 v233, v233, s14, v130
	v_add_u32_e32 v127, -9, v156
	v_and_or_b32 v234, v234, s14, v127
	v_add_u32_e32 v130, -10, v156
	v_and_or_b32 v235, v235, s14, v130
	v_add_u32_e32 v127, -11, v156
	v_and_or_b32 v236, v236, s14, v127
	v_add_u32_e32 v130, -12, v156
	v_and_or_b32 v237, v237, s14, v130
	v_max_f32_e32 v254, v222, v223
	v_min_f32_e32 v223, v222, v223
	v_max_f32_e32 v222, v224, v225
	v_min_f32_e32 v225, v224, v225
	v_max_f32_e32 v224, v254, v222
	v_min_f32_e32 v222, v254, v222
	v_max_f32_e32 v254, v223, v225
	v_min_f32_e32 v225, v223, v225
	v_max_f32_e32 v223, v254, v222
	v_min_f32_e32 v222, v254, v222
	v_max_f32_e32 v254, v226, v227
	v_min_f32_e32 v227, v226, v227
	v_max_f32_e32 v226, v228, v229
	v_min_f32_e32 v229, v228, v229
	v_max_f32_e32 v228, v254, v226
	v_min_f32_e32 v226, v254, v226
	v_max_f32_e32 v254, v227, v229
	v_min_f32_e32 v229, v227, v229
	v_max_f32_e32 v227, v254, v226
	v_min_f32_e32 v226, v254, v226
	v_max_f32_e32 v254, v224, v228
	v_min_f32_e32 v228, v224, v228
	v_max_f32_e32 v224, v222, v226
	v_min_f32_e32 v226, v222, v226
	v_max_f32_e32 v222, v224, v228
	v_min_f32_e32 v228, v224, v228
	v_max_f32_e32 v224, v223, v227
	v_min_f32_e32 v227, v223, v227
	v_max_f32_e32 v223, v225, v229
	v_min_f32_e32 v229, v225, v229
	v_max_f32_e32 v225, v223, v227
	v_min_f32_e32 v227, v223, v227
	v_max_f32_e32 v223, v224, v222
	v_min_f32_e32 v222, v224, v222
	v_max_f32_e32 v224, v225, v228
	v_min_f32_e32 v228, v225, v228
	v_max_f32_e32 v225, v227, v226
	v_min_f32_e32 v226, v227, v226
	v_max_f32_e32 v227, v230, v231
	v_min_f32_e32 v231, v230, v231
	v_max_f32_e32 v230, v232, v233
	v_min_f32_e32 v233, v232, v233
	v_max_f32_e32 v232, v227, v230
	v_min_f32_e32 v230, v227, v230
	v_max_f32_e32 v227, v231, v233
	v_min_f32_e32 v233, v231, v233
	v_max_f32_e32 v231, v227, v230
	v_min_f32_e32 v230, v227, v230
	v_max_f32_e32 v227, v234, v235
	v_min_f32_e32 v235, v234, v235
	v_max_f32_e32 v234, v236, v237
	v_min_f32_e32 v237, v236, v237
	v_max_f32_e32 v236, v227, v234
	v_min_f32_e32 v234, v227, v234
	v_max_f32_e32 v227, v235, v237
	v_min_f32_e32 v237, v235, v237
	v_max_f32_e32 v235, v227, v234
	v_min_f32_e32 v234, v227, v234
	v_max_f32_e32 v227, v232, v236
	v_min_f32_e32 v236, v232, v236
	v_max_f32_e32 v232, v230, v234
	v_min_f32_e32 v234, v230, v234
	v_max_f32_e32 v230, v232, v236
	v_min_f32_e32 v236, v232, v236
	v_max_f32_e32 v232, v231, v235
	v_min_f32_e32 v235, v231, v235
	v_max_f32_e32 v231, v233, v237
	v_min_f32_e32 v237, v233, v237
	v_max_f32_e32 v233, v231, v235
	v_min_f32_e32 v235, v231, v235
	v_max_f32_e32 v231, v232, v230
	v_min_f32_e32 v230, v232, v230
	v_max_f32_e32 v232, v233, v236
	v_min_f32_e32 v236, v233, v236
	v_max_f32_e32 v233, v235, v234
	v_min_f32_e32 v234, v235, v234
	v_max_f32_e32 v235, v254, v227
	v_min_f32_e32 v227, v254, v227
	v_max_f32_e32 v254, v228, v236
	v_min_f32_e32 v236, v228, v236
	v_max_f32_e32 v228, v254, v227
	v_min_f32_e32 v227, v254, v227
; #define LAS __attribute__((address_space(3)))
; __device__ __forceinline__ float uniq_key(float s, int n) { return __uint_as_float((__float_as_uint(s) & ~0xffu) | (unsigned)(255 - n)); }
; #define INS16(A_, X_) do { float x_ = (X_); _Pragma("unroll") for (int i_ = 0; i_ < 16; ++i_) { const float hi_ = fmaxf(A_[i_], x_); x_ = fminf(A_[i_], x_); A_[i_] = hi_; } } while (0)
; __device__ __forceinline__ void p11_route(Frame& F) {
;     ...
;         { LAS float* row = sc + (F.lane & 31) * 129; float a[16]; const int nb = (F.lane >> 5) * (PNK / 2);
; #pragma unroll
;             for (int i = 0; i < 16; ++i) a[i] = -INFINITY;
; #pragma unroll 4
;             for (int n = 0; n < PNK / 2; ++n) INS16(a, uniq_key(row[nb + n], nb + n));
	v_max_f32_e32 v254, v222, v230
	v_min_f32_e32 v230, v222, v230
	v_max_f32_e32 v222, v226, v234
	v_min_f32_e32 v234, v226, v234
	v_max_f32_e32 v226, v222, v230
	v_min_f32_e32 v230, v222, v230
	v_max_f32_e32 v222, v254, v228
	v_min_f32_e32 v228, v254, v228
	v_max_f32_e32 v254, v226, v227
	v_min_f32_e32 v227, v226, v227
	v_max_f32_e32 v226, v230, v236
	v_min_f32_e32 v236, v230, v236
	v_max_f32_e32 v230, v223, v231
	v_min_f32_e32 v231, v223, v231
	v_max_f32_e32 v223, v225, v233
	v_min_f32_e32 v233, v225, v233
	v_max_f32_e32 v225, v223, v231
	v_min_f32_e32 v231, v223, v231
	v_max_f32_e32 v223, v224, v232
	v_min_f32_e32 v232, v224, v232
	v_max_f32_e32 v224, v229, v237
	v_min_f32_e32 v237, v229, v237
	v_max_f32_e32 v229, v224, v232
	v_min_f32_e32 v232, v224, v232
	v_max_f32_e32 v224, v223, v225
	v_min_f32_e32 v225, v223, v225
	v_max_f32_e32 v223, v229, v231
	v_min_f32_e32 v231, v229, v231
	v_max_f32_e32 v229, v232, v233
	v_min_f32_e32 v233, v232, v233
	v_max_f32_e32 v232, v230, v222
	v_min_f32_e32 v222, v230, v222
	v_max_f32_e32 v230, v224, v228
	v_min_f32_e32 v228, v224, v228
	v_max_f32_e32 v224, v225, v254
	v_min_f32_e32 v254, v225, v254
	v_max_f32_e32 v225, v223, v227
	v_min_f32_e32 v227, v223, v227
	v_max_f32_e32 v223, v231, v226
	v_min_f32_e32 v226, v231, v226
	v_max_f32_e32 v231, v229, v236
	v_min_f32_e32 v236, v229, v236
	v_max_f32_e32 v229, v233, v234
	v_min_f32_e32 v234, v233, v234
	s_waitcnt lgkmcnt(0)
	v_add_u32_e32 v127, -13, v156
	v_and_or_b32 v238, v238, s14, v127
	v_add_u32_e32 v130, -14, v156
	v_and_or_b32 v239, v239, s14, v130
	v_add_u32_e32 v127, -15, v156
	v_and_or_b32 v240, v240, s14, v127
	v_add_u32_e32 v130, -16, v156
	v_and_or_b32 v241, v241, s14, v130
	v_add_u32_e32 v127, 0xffffffef, v156
	v_and_or_b32 v242, v242, s14, v127
	v_add_u32_e32 v130, 0xffffffee, v156
	v_and_or_b32 v243, v243, s14, v130
	v_add_u32_e32 v127, 0xffffffed, v156
	v_and_or_b32 v244, v244, s14, v127
	v_add_u32_e32 v130, 0xffffffec, v156
	v_and_or_b32 v245, v245, s14, v130
	v_add_u32_e32 v127, 0xffffffeb, v156
	v_and_or_b32 v246, v246, s14, v127
	v_add_u32_e32 v130, 0xffffffea, v156
	v_and_or_b32 v247, v247, s14, v130
	v_add_u32_e32 v127, 0xffffffe9, v156
	v_and_or_b32 v248, v248, s14, v127
	v_add_u32_e32 v130, 0xffffffe8, v156
	v_and_or_b32 v249, v249, s14, v130
	v_add_u32_e32 v127, 0xffffffe7, v156
	v_and_or_b32 v250, v250, s14, v127
	v_add_u32_e32 v130, 0xffffffe6, v156
	v_and_or_b32 v251, v251, s14, v130
	v_add_u32_e32 v127, 0xffffffe5, v156
	v_and_or_b32 v252, v252, s14, v127
	v_add_u32_e32 v130, 0xffffffe4, v156
	v_and_or_b32 v253, v253, s14, v130
	v_max_f32_e32 v128, v238, v239
	v_min_f32_e32 v239, v238, v239
	v_max_f32_e32 v238, v240, v241
	v_min_f32_e32 v241, v240, v241
	v_max_f32_e32 v240, v128, v238
	v_min_f32_e32 v238, v128, v238
	v_max_f32_e32 v128, v239, v241
	v_min_f32_e32 v241, v239, v241
	v_max_f32_e32 v239, v128, v238
	v_min_f32_e32 v238, v128, v238
	v_max_f32_e32 v128, v242, v243
	v_min_f32_e32 v243, v242, v243
	v_max_f32_e32 v242, v244, v245
	v_min_f32_e32 v245, v244, v245
	v_max_f32_e32 v244, v128, v242
	v_min_f32_e32 v242, v128, v242
	v_max_f32_e32 v128, v243, v245
	v_min_f32_e32 v245, v243, v245
	v_max_f32_e32 v243, v128, v242
	v_min_f32_e32 v242, v128, v242
	v_max_f32_e32 v128, v240, v244
	v_min_f32_e32 v244, v240, v244
	v_max_f32_e32 v240, v238, v242
	v_min_f32_e32 v242, v238, v242
	v_max_f32_e32 v238, v240, v244
	v_min_f32_e32 v244, v240, v244
	v_max_f32_e32 v240, v239, v243
	v_min_f32_e32 v243, v239, v243
	v_max_f32_e32 v239, v241, v245
	v_min_f32_e32 v245, v241, v245
	v_max_f32_e32 v241, v239, v243
	v_min_f32_e32 v243, v239, v243
	v_max_f32_e32 v239, v240, v238
	v_min_f32_e32 v238, v240, v238
	v_max_f32_e32 v240, v241, v244
	v_min_f32_e32 v244, v241, v244
	v_max_f32_e32 v241, v243, v242
	v_min_f32_e32 v242, v243, v242
	v_max_f32_e32 v243, v246, v247
	v_min_f32_e32 v247, v246, v247
	v_max_f32_e32 v246, v248, v249
	v_min_f32_e32 v249, v248, v249
	v_max_f32_e32 v248, v243, v246
	v_min_f32_e32 v246, v243, v246
	v_max_f32_e32 v243, v247, v249
	v_min_f32_e32 v249, v247, v249
	v_max_f32_e32 v247, v243, v246
	v_min_f32_e32 v246, v243, v246
	v_max_f32_e32 v243, v250, v251
	v_min_f32_e32 v251, v250, v251
	v_max_f32_e32 v250, v252, v253
	v_min_f32_e32 v253, v252, v253
	v_max_f32_e32 v252, v243, v250
	v_min_f32_e32 v250, v243, v250
	v_max_f32_e32 v243, v251, v253
	v_min_f32_e32 v253, v251, v253
	v_max_f32_e32 v251, v243, v250
	v_min_f32_e32 v250, v243, v250
	v_max_f32_e32 v243, v248, v252
	v_min_f32_e32 v252, v248, v252
	v_max_f32_e32 v248, v246, v250
	v_min_f32_e32 v250, v246, v250
	v_max_f32_e32 v246, v248, v252
	v_min_f32_e32 v252, v248, v252
	v_max_f32_e32 v248, v247, v251
	v_min_f32_e32 v251, v247, v251
	v_max_f32_e32 v247, v249, v253
	v_min_f32_e32 v253, v249, v253
	v_max_f32_e32 v249, v247, v251
	v_min_f32_e32 v251, v247, v251
	v_max_f32_e32 v247, v248, v246
	v_min_f32_e32 v246, v248, v246
	v_max_f32_e32 v248, v249, v252
	v_min_f32_e32 v252, v249, v252
	v_max_f32_e32 v249, v251, v250
	v_min_f32_e32 v250, v251, v250
	v_max_f32_e32 v251, v128, v243
	v_min_f32_e32 v243, v128, v243
	v_max_f32_e32 v128, v244, v252
	v_min_f32_e32 v252, v244, v252
	v_max_f32_e32 v244, v128, v243
	v_min_f32_e32 v243, v128, v243
	v_max_f32_e32 v128, v238, v246
	v_min_f32_e32 v246, v238, v246
	v_max_f32_e32 v238, v242, v250
	v_min_f32_e32 v250, v242, v250
	v_max_f32_e32 v242, v238, v246
	v_min_f32_e32 v246, v238, v246
	v_max_f32_e32 v238, v128, v244
	v_min_f32_e32 v244, v128, v244
	v_max_f32_e32 v128, v242, v243
	v_min_f32_e32 v243, v242, v243
	v_max_f32_e32 v242, v246, v252
	v_min_f32_e32 v252, v246, v252
	v_max_f32_e32 v246, v239, v247
; #define LAS __attribute__((address_space(3)))
; __device__ __forceinline__ float uniq_key(float s, int n) { return __uint_as_float((__float_as_uint(s) & ~0xffu) | (unsigned)(255 - n)); }
; #define INS16(A_, X_) do { float x_ = (X_); _Pragma("unroll") for (int i_ = 0; i_ < 16; ++i_) { const float hi_ = fmaxf(A_[i_], x_); x_ = fminf(A_[i_], x_); A_[i_] = hi_; } } while (0)
; __device__ __forceinline__ void p11_route(Frame& F) {
;     ...
;         { LAS float* row = sc + (F.lane & 31) * 129; float a[16]; const int nb = (F.lane >> 5) * (PNK / 2);
; #pragma unroll
;             for (int i = 0; i < 16; ++i) a[i] = -INFINITY;
; #pragma unroll 4
;             for (int n = 0; n < PNK / 2; ++n) INS16(a, uniq_key(row[nb + n], nb + n));
	v_min_f32_e32 v247, v239, v247
	v_max_f32_e32 v239, v241, v249
	v_min_f32_e32 v249, v241, v249
	v_max_f32_e32 v241, v239, v247
	v_min_f32_e32 v247, v239, v247
	v_max_f32_e32 v239, v240, v248
	v_min_f32_e32 v248, v240, v248
	v_max_f32_e32 v240, v245, v253
	v_min_f32_e32 v253, v245, v253
	v_max_f32_e32 v245, v240, v248
	v_min_f32_e32 v248, v240, v248
	v_max_f32_e32 v240, v239, v241
	v_min_f32_e32 v241, v239, v241
	v_max_f32_e32 v239, v245, v247
	v_min_f32_e32 v247, v245, v247
	v_max_f32_e32 v245, v248, v249
	v_min_f32_e32 v249, v248, v249
	v_max_f32_e32 v248, v246, v238
	v_min_f32_e32 v238, v246, v238
	v_max_f32_e32 v246, v240, v244
	v_min_f32_e32 v244, v240, v244
	v_max_f32_e32 v240, v241, v128
	v_min_f32_e32 v128, v241, v128
	v_max_f32_e32 v241, v239, v243
	v_min_f32_e32 v243, v239, v243
	v_max_f32_e32 v239, v247, v242
	v_min_f32_e32 v242, v247, v242
	v_max_f32_e32 v247, v245, v252
	v_min_f32_e32 v252, v245, v252
	v_max_f32_e32 v245, v249, v250
	v_min_f32_e32 v250, v249, v250
	v_max_f32_e32 v235, v235, v253
	v_max_f32_e32 v232, v232, v250
	v_max_f32_e32 v222, v222, v245
	v_max_f32_e32 v230, v230, v252
	v_max_f32_e32 v228, v228, v247
	v_max_f32_e32 v224, v224, v242
	v_max_f32_e32 v254, v254, v239
	v_max_f32_e32 v225, v225, v243
	v_max_f32_e32 v227, v227, v241
	v_max_f32_e32 v223, v223, v128
	v_max_f32_e32 v226, v226, v240
	v_max_f32_e32 v231, v231, v244
	v_max_f32_e32 v236, v236, v246
	v_max_f32_e32 v229, v229, v238
	v_max_f32_e32 v234, v234, v248
	v_max_f32_e32 v237, v237, v251
	ds_read2_b32 v[238:239], v155 offset0:32 offset1:33
	ds_read2_b32 v[240:241], v155 offset0:34 offset1:35
	ds_read2_b32 v[242:243], v155 offset0:36 offset1:37
	ds_read2_b32 v[244:245], v155 offset0:38 offset1:39
	ds_read2_b32 v[246:247], v155 offset0:40 offset1:41
	ds_read2_b32 v[248:249], v155 offset0:42 offset1:43
	ds_read2_b32 v[250:251], v155 offset0:44 offset1:45
	ds_read2_b32 v[252:253], v155 offset0:46 offset1:47
	v_max_f32_e32 v233, v235, v227
	v_min_f32_e32 v227, v235, v227
	v_max_f32_e32 v235, v232, v223
	v_min_f32_e32 v223, v232, v223
	v_max_f32_e32 v232, v222, v226
	v_min_f32_e32 v226, v222, v226
	v_max_f32_e32 v222, v230, v231
	v_min_f32_e32 v231, v230, v231
	v_max_f32_e32 v230, v228, v236
	v_min_f32_e32 v236, v228, v236
	v_max_f32_e32 v228, v224, v229
	v_min_f32_e32 v229, v224, v229
	v_max_f32_e32 v224, v254, v234
	v_min_f32_e32 v234, v254, v234
	v_max_f32_e32 v254, v225, v237
	v_min_f32_e32 v237, v225, v237
	v_max_f32_e32 v225, v233, v230
	v_min_f32_e32 v230, v233, v230
	v_max_f32_e32 v233, v235, v228
	v_min_f32_e32 v228, v235, v228
	v_max_f32_e32 v235, v232, v224
	v_min_f32_e32 v224, v232, v224
	v_max_f32_e32 v232, v222, v254
	v_min_f32_e32 v254, v222, v254
	v_max_f32_e32 v222, v227, v236
	v_min_f32_e32 v236, v227, v236
	v_max_f32_e32 v227, v223, v229
	v_min_f32_e32 v229, v223, v229
	v_max_f32_e32 v223, v226, v234
	v_min_f32_e32 v234, v226, v234
	v_max_f32_e32 v226, v231, v237
	v_min_f32_e32 v237, v231, v237
	v_max_f32_e32 v231, v225, v235
	v_min_f32_e32 v235, v225, v235
	v_max_f32_e32 v225, v233, v232
	v_min_f32_e32 v232, v233, v232
	v_max_f32_e32 v233, v230, v224
	v_min_f32_e32 v224, v230, v224
	v_max_f32_e32 v230, v228, v254
	v_min_f32_e32 v254, v228, v254
	v_max_f32_e32 v228, v222, v223
	v_min_f32_e32 v223, v222, v223
	v_max_f32_e32 v222, v227, v226
	v_min_f32_e32 v226, v227, v226
	v_max_f32_e32 v227, v236, v234
	v_min_f32_e32 v234, v236, v234
	v_max_f32_e32 v236, v229, v237
	v_min_f32_e32 v237, v229, v237
	v_max_f32_e32 v229, v231, v225
	v_min_f32_e32 v225, v231, v225
	v_max_f32_e32 v231, v235, v232
	v_min_f32_e32 v232, v235, v232
	v_max_f32_e32 v235, v233, v230
	v_min_f32_e32 v230, v233, v230
	v_max_f32_e32 v233, v224, v254
	v_min_f32_e32 v254, v224, v254
	v_max_f32_e32 v224, v228, v222
	v_min_f32_e32 v222, v228, v222
	v_max_f32_e32 v228, v223, v226
	v_min_f32_e32 v226, v223, v226
	v_max_f32_e32 v223, v227, v236
	v_min_f32_e32 v236, v227, v236
	v_max_f32_e32 v227, v234, v237
	v_min_f32_e32 v237, v234, v237
	s_waitcnt lgkmcnt(0)
	v_add_u32_e32 v127, 0xffffffe3, v156
	v_and_or_b32 v238, v238, s14, v127
	v_add_u32_e32 v130, 0xffffffe2, v156
	v_and_or_b32 v239, v239, s14, v130
	v_add_u32_e32 v127, 0xffffffe1, v156
	v_and_or_b32 v240, v240, s14, v127
	v_add_u32_e32 v130, 0xffffffe0, v156
	v_and_or_b32 v241, v241, s14, v130
	v_add_u32_e32 v127, 0xffffffdf, v156
	v_and_or_b32 v242, v242, s14, v127
	v_add_u32_e32 v130, 0xffffffde, v156
	v_and_or_b32 v243, v243, s14, v130
	v_add_u32_e32 v127, 0xffffffdd, v156
	v_and_or_b32 v244, v244, s14, v127
	v_add_u32_e32 v130, 0xffffffdc, v156
	v_and_or_b32 v245, v245, s14, v130
	v_add_u32_e32 v127, 0xffffffdb, v156
	v_and_or_b32 v246, v246, s14, v127
	v_add_u32_e32 v130, 0xffffffda, v156
	v_and_or_b32 v247, v247, s14, v130
	v_add_u32_e32 v127, 0xffffffd9, v156
	v_and_or_b32 v248, v248, s14, v127
	v_add_u32_e32 v130, 0xffffffd8, v156
	v_and_or_b32 v249, v249, s14, v130
	v_add_u32_e32 v127, 0xffffffd7, v156
	v_and_or_b32 v250, v250, s14, v127
	v_add_u32_e32 v130, 0xffffffd6, v156
	v_and_or_b32 v251, v251, s14, v130
	v_add_u32_e32 v127, 0xffffffd5, v156
	v_and_or_b32 v252, v252, s14, v127
	v_add_u32_e32 v130, 0xffffffd4, v156
	v_and_or_b32 v253, v253, s14, v130
	v_max_f32_e32 v128, v238, v239
	v_min_f32_e32 v239, v238, v239
	v_max_f32_e32 v238, v240, v241
	v_min_f32_e32 v241, v240, v241
	v_max_f32_e32 v240, v128, v238
	v_min_f32_e32 v238, v128, v238
	v_max_f32_e32 v128, v239, v241
	v_min_f32_e32 v241, v239, v241
	v_max_f32_e32 v239, v128, v238
	v_min_f32_e32 v238, v128, v238
	v_max_f32_e32 v128, v242, v243
	v_min_f32_e32 v243, v242, v243
	v_max_f32_e32 v242, v244, v245
	v_min_f32_e32 v245, v244, v245
; #define LAS __attribute__((address_space(3)))
; __device__ __forceinline__ float uniq_key(float s, int n) { return __uint_as_float((__float_as_uint(s) & ~0xffu) | (unsigned)(255 - n)); }
; #define INS16(A_, X_) do { float x_ = (X_); _Pragma("unroll") for (int i_ = 0; i_ < 16; ++i_) { const float hi_ = fmaxf(A_[i_], x_); x_ = fminf(A_[i_], x_); A_[i_] = hi_; } } while (0)
; __device__ __forceinline__ void p11_route(Frame& F) {
;     ...
;         { LAS float* row = sc + (F.lane & 31) * 129; float a[16]; const int nb = (F.lane >> 5) * (PNK / 2);
; #pragma unroll
;             for (int i = 0; i < 16; ++i) a[i] = -INFINITY;
; #pragma unroll 4
;             for (int n = 0; n < PNK / 2; ++n) INS16(a, uniq_key(row[nb + n], nb + n));
	v_max_f32_e32 v244, v128, v242
	v_min_f32_e32 v242, v128, v242
	v_max_f32_e32 v128, v243, v245
	v_min_f32_e32 v245, v243, v245
	v_max_f32_e32 v243, v128, v242
	v_min_f32_e32 v242, v128, v242
	v_max_f32_e32 v128, v240, v244
	v_min_f32_e32 v244, v240, v244
	v_max_f32_e32 v240, v238, v242
	v_min_f32_e32 v242, v238, v242
	v_max_f32_e32 v238, v240, v244
	v_min_f32_e32 v244, v240, v244
	v_max_f32_e32 v240, v239, v243
	v_min_f32_e32 v243, v239, v243
	v_max_f32_e32 v239, v241, v245
	v_min_f32_e32 v245, v241, v245
	v_max_f32_e32 v241, v239, v243
	v_min_f32_e32 v243, v239, v243
	v_max_f32_e32 v239, v240, v238
	v_min_f32_e32 v238, v240, v238
	v_max_f32_e32 v240, v241, v244
	v_min_f32_e32 v244, v241, v244
	v_max_f32_e32 v241, v243, v242
	v_min_f32_e32 v242, v243, v242
	v_max_f32_e32 v243, v246, v247
	v_min_f32_e32 v247, v246, v247
	v_max_f32_e32 v246, v248, v249
	v_min_f32_e32 v249, v248, v249
	v_max_f32_e32 v248, v243, v246
	v_min_f32_e32 v246, v243, v246
	v_max_f32_e32 v243, v247, v249
	v_min_f32_e32 v249, v247, v249
	v_max_f32_e32 v247, v243, v246
	v_min_f32_e32 v246, v243, v246
	v_max_f32_e32 v243, v250, v251
	v_min_f32_e32 v251, v250, v251
	v_max_f32_e32 v250, v252, v253
	v_min_f32_e32 v253, v252, v253
	v_max_f32_e32 v252, v243, v250
	v_min_f32_e32 v250, v243, v250
	v_max_f32_e32 v243, v251, v253
	v_min_f32_e32 v253, v251, v253
	v_max_f32_e32 v251, v243, v250
	v_min_f32_e32 v250, v243, v250
	v_max_f32_e32 v243, v248, v252
	v_min_f32_e32 v252, v248, v252
	v_max_f32_e32 v248, v246, v250
	v_min_f32_e32 v250, v246, v250
	v_max_f32_e32 v246, v248, v252
	v_min_f32_e32 v252, v248, v252
	v_max_f32_e32 v248, v247, v251
	v_min_f32_e32 v251, v247, v251
	v_max_f32_e32 v247, v249, v253
	v_min_f32_e32 v253, v249, v253
	v_max_f32_e32 v249, v247, v251
	v_min_f32_e32 v251, v247, v251
	v_max_f32_e32 v247, v248, v246
	v_min_f32_e32 v246, v248, v246
	v_max_f32_e32 v248, v249, v252
	v_min_f32_e32 v252, v249, v252
	v_max_f32_e32 v249, v251, v250
	v_min_f32_e32 v250, v251, v250
	v_max_f32_e32 v251, v128, v243
	v_min_f32_e32 v243, v128, v243
	v_max_f32_e32 v128, v244, v252
	v_min_f32_e32 v252, v244, v252
	v_max_f32_e32 v244, v128, v243
	v_min_f32_e32 v243, v128, v243
	v_max_f32_e32 v128, v238, v246
	v_min_f32_e32 v246, v238, v246
	v_max_f32_e32 v238, v242, v250
	v_min_f32_e32 v250, v242, v250
	v_max_f32_e32 v242, v238, v246
	v_min_f32_e32 v246, v238, v246
	v_max_f32_e32 v238, v128, v244
	v_min_f32_e32 v244, v128, v244
	v_max_f32_e32 v128, v242, v243
	v_min_f32_e32 v243, v242, v243
	v_max_f32_e32 v242, v246, v252
	v_min_f32_e32 v252, v246, v252
	v_max_f32_e32 v246, v239, v247
	v_min_f32_e32 v247, v239, v247
	v_max_f32_e32 v239, v241, v249
	v_min_f32_e32 v249, v241, v249
	v_max_f32_e32 v241, v239, v247
	v_min_f32_e32 v247, v239, v247
	v_max_f32_e32 v239, v240, v248
	v_min_f32_e32 v248, v240, v248
	v_max_f32_e32 v240, v245, v253
	v_min_f32_e32 v253, v245, v253
	v_max_f32_e32 v245, v240, v248
	v_min_f32_e32 v248, v240, v248
	v_max_f32_e32 v240, v239, v241
	v_min_f32_e32 v241, v239, v241
	v_max_f32_e32 v239, v245, v247
	v_min_f32_e32 v247, v245, v247
	v_max_f32_e32 v245, v248, v249
	v_min_f32_e32 v249, v248, v249
	v_max_f32_e32 v248, v246, v238
	v_min_f32_e32 v238, v246, v238
	v_max_f32_e32 v246, v240, v244
	v_min_f32_e32 v244, v240, v244
	v_max_f32_e32 v240, v241, v128
	v_min_f32_e32 v128, v241, v128
	v_max_f32_e32 v241, v239, v243
	v_min_f32_e32 v243, v239, v243
	v_max_f32_e32 v239, v247, v242
	v_min_f32_e32 v242, v247, v242
	v_max_f32_e32 v247, v245, v252
	v_min_f32_e32 v252, v245, v252
	v_max_f32_e32 v245, v249, v250
	v_min_f32_e32 v250, v249, v250
	v_max_f32_e32 v229, v229, v253
	v_max_f32_e32 v225, v225, v250
	v_max_f32_e32 v231, v231, v245
	v_max_f32_e32 v232, v232, v252
	v_max_f32_e32 v235, v235, v247
	v_max_f32_e32 v230, v230, v242
	v_max_f32_e32 v233, v233, v239
	v_max_f32_e32 v254, v254, v243
	v_max_f32_e32 v224, v224, v241
	v_max_f32_e32 v222, v222, v128
	v_max_f32_e32 v228, v228, v240
	v_max_f32_e32 v226, v226, v244
	v_max_f32_e32 v223, v223, v246
	v_max_f32_e32 v236, v236, v238
	v_max_f32_e32 v227, v227, v248
	v_max_f32_e32 v237, v237, v251
	ds_read2_b32 v[238:239], v155 offset0:48 offset1:49
	ds_read2_b32 v[240:241], v155 offset0:50 offset1:51
	ds_read2_b32 v[242:243], v155 offset0:52 offset1:53
	ds_read2_b32 v[244:245], v155 offset0:54 offset1:55
	ds_read2_b32 v[246:247], v155 offset0:56 offset1:57
	ds_read2_b32 v[248:249], v155 offset0:58 offset1:59
	ds_read2_b32 v[250:251], v155 offset0:60 offset1:61
	ds_read2_b32 v[252:253], v155 offset0:62 offset1:63
	v_max_f32_e32 v234, v229, v224
	v_min_f32_e32 v224, v229, v224
	v_max_f32_e32 v229, v225, v222
	v_min_f32_e32 v222, v225, v222
	v_max_f32_e32 v225, v231, v228
	v_min_f32_e32 v228, v231, v228
	v_max_f32_e32 v231, v232, v226
	v_min_f32_e32 v226, v232, v226
	v_max_f32_e32 v232, v235, v223
	v_min_f32_e32 v223, v235, v223
	v_max_f32_e32 v235, v230, v236
	v_min_f32_e32 v236, v230, v236
	v_max_f32_e32 v230, v233, v227
	v_min_f32_e32 v227, v233, v227
	v_max_f32_e32 v233, v254, v237
	v_min_f32_e32 v237, v254, v237
	v_max_f32_e32 v254, v234, v232
	v_min_f32_e32 v232, v234, v232
	v_max_f32_e32 v234, v229, v235
	v_min_f32_e32 v235, v229, v235
	v_max_f32_e32 v229, v225, v230
	v_min_f32_e32 v230, v225, v230
	v_max_f32_e32 v225, v231, v233
	v_min_f32_e32 v233, v231, v233
	v_max_f32_e32 v231, v224, v223
	v_min_f32_e32 v223, v224, v223
	v_max_f32_e32 v224, v222, v236
	v_min_f32_e32 v236, v222, v236
	v_max_f32_e32 v222, v228, v227
	v_min_f32_e32 v227, v228, v227
	v_max_f32_e32 v228, v226, v237
	v_min_f32_e32 v237, v226, v237
	v_max_f32_e32 v226, v254, v229
	v_min_f32_e32 v229, v254, v229
	v_max_f32_e32 v254, v234, v225
	v_min_f32_e32 v225, v234, v225
	v_max_f32_e32 v234, v232, v230
	v_min_f32_e32 v230, v232, v230
	v_max_f32_e32 v232, v235, v233
	v_min_f32_e32 v233, v235, v233
	v_max_f32_e32 v235, v231, v222
	v_min_f32_e32 v222, v231, v222
	v_max_f32_e32 v231, v224, v228
	v_min_f32_e32 v228, v224, v228
	v_max_f32_e32 v224, v223, v227
	v_min_f32_e32 v227, v223, v227
	v_max_f32_e32 v223, v236, v237
	v_min_f32_e32 v237, v236, v237
	v_max_f32_e32 v236, v226, v254
	v_min_f32_e32 v254, v226, v254
	v_max_f32_e32 v226, v229, v225
	v_min_f32_e32 v225, v229, v225
	v_max_f32_e32 v229, v234, v232
	v_min_f32_e32 v232, v234, v232
	v_max_f32_e32 v234, v230, v233
	v_min_f32_e32 v233, v230, v233
	v_max_f32_e32 v230, v235, v231
	v_min_f32_e32 v231, v235, v231
	v_max_f32_e32 v235, v222, v228
	v_min_f32_e32 v228, v222, v228
	v_max_f32_e32 v222, v224, v223
	v_min_f32_e32 v223, v224, v223
	v_max_f32_e32 v224, v227, v237
	v_min_f32_e32 v237, v227, v237
	s_waitcnt lgkmcnt(0)
; #define LAS __attribute__((address_space(3)))
; __device__ __forceinline__ float uniq_key(float s, int n) { return __uint_as_float((__float_as_uint(s) & ~0xffu) | (unsigned)(255 - n)); }
; #define INS16(A_, X_) do { float x_ = (X_); _Pragma("unroll") for (int i_ = 0; i_ < 16; ++i_) { const float hi_ = fmaxf(A_[i_], x_); x_ = fminf(A_[i_], x_); A_[i_] = hi_; } } while (0)
; __device__ __forceinline__ void p11_route(Frame& F) {
;     ...
;         { LAS float* row = sc + (F.lane & 31) * 129; float a[16]; const int nb = (F.lane >> 5) * (PNK / 2);
; #pragma unroll
;             for (int i = 0; i < 16; ++i) a[i] = -INFINITY;
; #pragma unroll 4
;             for (int n = 0; n < PNK / 2; ++n) INS16(a, uniq_key(row[nb + n], nb + n));
	v_add_u32_e32 v127, 0xffffffd3, v156
	v_and_or_b32 v238, v238, s14, v127
	v_add_u32_e32 v130, 0xffffffd2, v156
	v_and_or_b32 v239, v239, s14, v130
	v_add_u32_e32 v127, 0xffffffd1, v156
	v_and_or_b32 v240, v240, s14, v127
	v_add_u32_e32 v130, 0xffffffd0, v156
	v_and_or_b32 v241, v241, s14, v130
	v_add_u32_e32 v127, 0xffffffcf, v156
	v_and_or_b32 v242, v242, s14, v127
	v_add_u32_e32 v130, 0xffffffce, v156
	v_and_or_b32 v243, v243, s14, v130
	v_add_u32_e32 v127, 0xffffffcd, v156
	v_and_or_b32 v244, v244, s14, v127
	v_add_u32_e32 v130, 0xffffffcc, v156
	v_and_or_b32 v245, v245, s14, v130
	v_add_u32_e32 v127, 0xffffffcb, v156
	v_and_or_b32 v246, v246, s14, v127
	v_add_u32_e32 v130, 0xffffffca, v156
	v_and_or_b32 v247, v247, s14, v130
	v_add_u32_e32 v127, 0xffffffc9, v156
	v_and_or_b32 v248, v248, s14, v127
	v_add_u32_e32 v130, 0xffffffc8, v156
	v_and_or_b32 v249, v249, s14, v130
	v_add_u32_e32 v127, 0xffffffc7, v156
	v_and_or_b32 v250, v250, s14, v127
	v_add_u32_e32 v130, 0xffffffc6, v156
	v_and_or_b32 v251, v251, s14, v130
	v_add_u32_e32 v127, 0xffffffc5, v156
	v_and_or_b32 v252, v252, s14, v127
	v_add_u32_e32 v130, 0xffffffc4, v156
	v_and_or_b32 v253, v253, s14, v130
	v_max_f32_e32 v128, v238, v239
	v_min_f32_e32 v239, v238, v239
	v_max_f32_e32 v238, v240, v241
	v_min_f32_e32 v241, v240, v241
	v_max_f32_e32 v240, v128, v238
	v_min_f32_e32 v238, v128, v238
	v_max_f32_e32 v128, v239, v241
	v_min_f32_e32 v241, v239, v241
	v_max_f32_e32 v239, v128, v238
	v_min_f32_e32 v238, v128, v238
	v_max_f32_e32 v128, v242, v243
	v_min_f32_e32 v243, v242, v243
	v_max_f32_e32 v242, v244, v245
	v_min_f32_e32 v245, v244, v245
	v_max_f32_e32 v244, v128, v242
	v_min_f32_e32 v242, v128, v242
	v_max_f32_e32 v128, v243, v245
	v_min_f32_e32 v245, v243, v245
	v_max_f32_e32 v243, v128, v242
	v_min_f32_e32 v242, v128, v242
	v_max_f32_e32 v128, v240, v244
	v_min_f32_e32 v244, v240, v244
	v_max_f32_e32 v240, v238, v242
	v_min_f32_e32 v242, v238, v242
	v_max_f32_e32 v238, v240, v244
	v_min_f32_e32 v244, v240, v244
	v_max_f32_e32 v240, v239, v243
	v_min_f32_e32 v243, v239, v243
	v_max_f32_e32 v239, v241, v245
	v_min_f32_e32 v245, v241, v245
	v_max_f32_e32 v241, v239, v243
	v_min_f32_e32 v243, v239, v243
	v_max_f32_e32 v239, v240, v238
	v_min_f32_e32 v238, v240, v238
	v_max_f32_e32 v240, v241, v244
	v_min_f32_e32 v244, v241, v244
	v_max_f32_e32 v241, v243, v242
	v_min_f32_e32 v242, v243, v242
	v_max_f32_e32 v243, v246, v247
	v_min_f32_e32 v247, v246, v247
	v_max_f32_e32 v246, v248, v249
	v_min_f32_e32 v249, v248, v249
	v_max_f32_e32 v248, v243, v246
	v_min_f32_e32 v246, v243, v246
	v_max_f32_e32 v243, v247, v249
	v_min_f32_e32 v249, v247, v249
	v_max_f32_e32 v247, v243, v246
	v_min_f32_e32 v246, v243, v246
	v_max_f32_e32 v243, v250, v251
	v_min_f32_e32 v251, v250, v251
	v_max_f32_e32 v250, v252, v253
	v_min_f32_e32 v253, v252, v253
	v_max_f32_e32 v252, v243, v250
	v_min_f32_e32 v250, v243, v250
	v_max_f32_e32 v243, v251, v253
	v_min_f32_e32 v253, v251, v253
	v_max_f32_e32 v251, v243, v250
	v_min_f32_e32 v250, v243, v250
	v_max_f32_e32 v243, v248, v252
	v_min_f32_e32 v252, v248, v252
	v_max_f32_e32 v248, v246, v250
	v_min_f32_e32 v250, v246, v250
	v_max_f32_e32 v246, v248, v252
	v_min_f32_e32 v252, v248, v252
	v_max_f32_e32 v248, v247, v251
	v_min_f32_e32 v251, v247, v251
	v_max_f32_e32 v247, v249, v253
	v_min_f32_e32 v253, v249, v253
	v_max_f32_e32 v249, v247, v251
	v_min_f32_e32 v251, v247, v251
	v_max_f32_e32 v247, v248, v246
	v_min_f32_e32 v246, v248, v246
	v_max_f32_e32 v248, v249, v252
	v_min_f32_e32 v252, v249, v252
	v_max_f32_e32 v249, v251, v250
	v_min_f32_e32 v250, v251, v250
	v_max_f32_e32 v251, v128, v243
	v_min_f32_e32 v243, v128, v243
	v_max_f32_e32 v128, v244, v252
	v_min_f32_e32 v252, v244, v252
	v_max_f32_e32 v244, v128, v243
	v_min_f32_e32 v243, v128, v243
	v_max_f32_e32 v128, v238, v246
	v_min_f32_e32 v246, v238, v246
	v_max_f32_e32 v238, v242, v250
	v_min_f32_e32 v250, v242, v250
	v_max_f32_e32 v242, v238, v246
	v_min_f32_e32 v246, v238, v246
	v_max_f32_e32 v238, v128, v244
	v_min_f32_e32 v244, v128, v244
	v_max_f32_e32 v128, v242, v243
	v_min_f32_e32 v243, v242, v243
	v_max_f32_e32 v242, v246, v252
	v_min_f32_e32 v252, v246, v252
	v_max_f32_e32 v246, v239, v247
	v_min_f32_e32 v247, v239, v247
	v_max_f32_e32 v239, v241, v249
	v_min_f32_e32 v249, v241, v249
	v_max_f32_e32 v241, v239, v247
	v_min_f32_e32 v247, v239, v247
	v_max_f32_e32 v239, v240, v248
	v_min_f32_e32 v248, v240, v248
	v_max_f32_e32 v240, v245, v253
	v_min_f32_e32 v253, v245, v253
	v_max_f32_e32 v245, v240, v248
	v_min_f32_e32 v248, v240, v248
	v_max_f32_e32 v240, v239, v241
	v_min_f32_e32 v241, v239, v241
	v_max_f32_e32 v239, v245, v247
	v_min_f32_e32 v247, v245, v247
	v_max_f32_e32 v245, v248, v249
	v_min_f32_e32 v249, v248, v249
	v_max_f32_e32 v248, v246, v238
	v_min_f32_e32 v238, v246, v238
	v_max_f32_e32 v246, v240, v244
	v_min_f32_e32 v244, v240, v244
	v_max_f32_e32 v240, v241, v128
	v_min_f32_e32 v128, v241, v128
	v_max_f32_e32 v241, v239, v243
	v_min_f32_e32 v243, v239, v243
	v_max_f32_e32 v239, v247, v242
	v_min_f32_e32 v242, v247, v242
	v_max_f32_e32 v247, v245, v252
	v_min_f32_e32 v252, v245, v252
	v_max_f32_e32 v245, v249, v250
	v_min_f32_e32 v250, v249, v250
	v_max_f32_e32 v236, v236, v253
	v_max_f32_e32 v254, v254, v250
	v_max_f32_e32 v226, v226, v245
	v_max_f32_e32 v225, v225, v252
	v_max_f32_e32 v229, v229, v247
	v_max_f32_e32 v232, v232, v242
	v_max_f32_e32 v234, v234, v239
	v_max_f32_e32 v233, v233, v243
	v_max_f32_e32 v230, v230, v241
	v_max_f32_e32 v231, v231, v128
	v_max_f32_e32 v235, v235, v240
	v_max_f32_e32 v228, v228, v244
	v_max_f32_e32 v222, v222, v246
; __device__ __forceinline__ float uniq_key(float s, int n) { return __uint_as_float((__float_as_uint(s) & ~0xffu) | (unsigned)(255 - n)); }
; #define INS16(A_, X_) do { float x_ = (X_); _Pragma("unroll") for (int i_ = 0; i_ < 16; ++i_) { const float hi_ = fmaxf(A_[i_], x_); x_ = fminf(A_[i_], x_); A_[i_] = hi_; } } while (0)
; __device__ __forceinline__ void p11_route(Frame& F) {
;     ...
;             for (int n = 0; n < PNK / 2; ++n) INS16(a, uniq_key(row[nb + n], nb + n));
;             float o[16];
; #pragma unroll
;             for (int i = 0; i < 16; ++i) o[i] = __builtin_bit_cast(float, __builtin_amdgcn_ds_bpermute(((F.lane + 32) & 63) << 2, __builtin_bit_cast(int, a[i])));
; #pragma unroll
;             for (int i = 0; i < 16; ++i) INS16(a, o[i]);
	v_max_f32_e32 v223, v223, v238
	v_max_f32_e32 v224, v224, v248
	v_max_f32_e32 v237, v237, v251
	v_max_f32_e32 v227, v236, v230
	v_min_f32_e32 v230, v236, v230
	v_max_f32_e32 v236, v254, v231
	v_min_f32_e32 v231, v254, v231
	v_max_f32_e32 v254, v226, v235
	v_min_f32_e32 v235, v226, v235
	v_max_f32_e32 v226, v225, v228
	v_min_f32_e32 v228, v225, v228
	v_max_f32_e32 v225, v229, v222
	v_min_f32_e32 v222, v229, v222
	v_max_f32_e32 v229, v232, v223
	v_min_f32_e32 v223, v232, v223
	v_max_f32_e32 v232, v234, v224
	v_min_f32_e32 v224, v234, v224
	v_max_f32_e32 v234, v233, v237
	v_min_f32_e32 v237, v233, v237
	v_max_f32_e32 v233, v227, v225
	v_min_f32_e32 v225, v227, v225
	v_max_f32_e32 v227, v236, v229
	v_min_f32_e32 v229, v236, v229
	v_max_f32_e32 v236, v254, v232
	v_min_f32_e32 v232, v254, v232
	v_max_f32_e32 v254, v226, v234
	v_min_f32_e32 v234, v226, v234
	v_max_f32_e32 v226, v230, v222
	v_min_f32_e32 v222, v230, v222
	v_max_f32_e32 v230, v231, v223
	v_min_f32_e32 v223, v231, v223
	v_max_f32_e32 v231, v235, v224
	v_min_f32_e32 v224, v235, v224
	v_max_f32_e32 v235, v228, v237
	v_min_f32_e32 v237, v228, v237
	v_max_f32_e32 v228, v233, v236
	v_min_f32_e32 v236, v233, v236
	v_max_f32_e32 v233, v227, v254
	v_min_f32_e32 v254, v227, v254
	v_max_f32_e32 v227, v225, v232
	v_min_f32_e32 v232, v225, v232
	v_max_f32_e32 v225, v229, v234
	v_min_f32_e32 v234, v229, v234
	v_max_f32_e32 v229, v226, v231
	v_min_f32_e32 v231, v226, v231
	v_max_f32_e32 v226, v230, v235
	v_min_f32_e32 v235, v230, v235
	v_max_f32_e32 v230, v222, v224
	v_min_f32_e32 v224, v222, v224
	v_max_f32_e32 v222, v223, v237
	v_min_f32_e32 v237, v223, v237
	v_max_f32_e32 v223, v228, v233
	v_min_f32_e32 v233, v228, v233
	v_max_f32_e32 v228, v236, v254
	v_min_f32_e32 v254, v236, v254
	v_max_f32_e32 v236, v227, v225
	v_min_f32_e32 v225, v227, v225
	v_max_f32_e32 v227, v232, v234
	v_min_f32_e32 v234, v232, v234
	v_max_f32_e32 v232, v229, v226
	v_min_f32_e32 v226, v229, v226
	v_max_f32_e32 v229, v231, v235
	v_min_f32_e32 v235, v231, v235
	v_max_f32_e32 v231, v230, v222
	v_min_f32_e32 v222, v230, v222
	v_max_f32_e32 v230, v224, v237
	v_min_f32_e32 v237, v224, v237
	v_mov_b32_e32 v137, v223
	v_mov_b32_e32 v139, v233
	v_mov_b32_e32 v140, v228
	v_mov_b32_e32 v141, v254
	v_mov_b32_e32 v142, v236
	v_mov_b32_e32 v143, v225
	v_mov_b32_e32 v144, v227
	v_mov_b32_e32 v145, v234
	v_mov_b32_e32 v147, v232
	v_mov_b32_e32 v148, v226
	v_mov_b32_e32 v149, v229
	v_mov_b32_e32 v159, v235
	v_mov_b32_e32 v161, v231
	v_mov_b32_e32 v162, v222
	v_mov_b32_e32 v160, v230
	v_mov_b32_e32 v129, v237
	ds_bpermute_b32 v166, v153, v137
	ds_bpermute_b32 v165, v153, v139
	ds_bpermute_b32 v164, v153, v140
	ds_bpermute_b32 v163, v153, v141
	ds_bpermute_b32 v146, v153, v142
	ds_bpermute_b32 v138, v153, v143
	ds_bpermute_b32 v136, v153, v144
	ds_bpermute_b32 v135, v153, v145
	ds_bpermute_b32 v134, v153, v147
	ds_bpermute_b32 v133, v153, v148
	ds_bpermute_b32 v132, v153, v149
	ds_bpermute_b32 v131, v153, v159
	ds_bpermute_b32 v130, v153, v161
	ds_bpermute_b32 v128, v153, v162
	ds_bpermute_b32 v127, v153, v160
	ds_bpermute_b32 v126, v153, v129
	s_and_saveexec_b64 s[4:5], s[0:1]
	s_cbranch_execz .LBB0_3218
	s_waitcnt lgkmcnt(14)
	v_max_f32_e32 v166, v166, v166
	v_max_f32_e32 v137, v137, v137
	v_min_f32_e32 v167, v137, v166
	v_max_f32_e32 v139, v139, v139
	v_max_f32_e32 v137, v137, v166
	v_max_f32_e32 v165, v165, v165
	v_min_f32_e32 v168, v139, v167
	v_max_f32_e32 v140, v140, v140
	v_max_f32_e32 v139, v139, v167
	v_min_f32_e32 v166, v137, v165
	v_max_f32_e32 v137, v137, v165
	s_waitcnt lgkmcnt(13)
	v_max_f32_e32 v164, v164, v164
	v_min_f32_e32 v169, v140, v168
	v_max_f32_e32 v141, v141, v141
	v_max_f32_e32 v140, v140, v168
	v_min_f32_e32 v167, v139, v166
	v_max_f32_e32 v139, v139, v166
	v_min_f32_e32 v165, v137, v164
	v_max_f32_e32 v137, v137, v164
	s_waitcnt lgkmcnt(12)
	v_max_f32_e32 v163, v163, v163
	v_min_f32_e32 v170, v141, v169
	v_max_f32_e32 v142, v142, v142
	v_max_f32_e32 v141, v141, v169
	v_min_f32_e32 v168, v140, v167
	v_max_f32_e32 v140, v140, v167
	v_min_f32_e32 v166, v139, v165
	v_max_f32_e32 v139, v139, v165
	v_min_f32_e32 v164, v137, v163
	v_max_f32_e32 v137, v137, v163
	s_waitcnt lgkmcnt(11)
	v_max_f32_e32 v146, v146, v146
	v_min_f32_e32 v171, v142, v170
	v_max_f32_e32 v143, v143, v143
	v_max_f32_e32 v142, v142, v170
	v_min_f32_e32 v169, v141, v168
	v_max_f32_e32 v141, v141, v168
	v_min_f32_e32 v167, v140, v166
	v_max_f32_e32 v140, v140, v166
	v_min_f32_e32 v165, v139, v164
	v_max_f32_e32 v139, v139, v164
	v_min_f32_e32 v163, v137, v146
	v_max_f32_e32 v137, v137, v146
	s_waitcnt lgkmcnt(10)
	v_max_f32_e32 v138, v138, v138
	v_min_f32_e32 v172, v143, v171
	v_max_f32_e32 v144, v144, v144
	v_max_f32_e32 v143, v143, v171
	v_min_f32_e32 v170, v142, v169
	v_max_f32_e32 v142, v142, v169
	v_min_f32_e32 v168, v141, v167
	v_max_f32_e32 v141, v141, v167
	v_min_f32_e32 v166, v140, v165
	v_max_f32_e32 v140, v140, v165
	v_min_f32_e32 v164, v139, v163
	v_max_f32_e32 v139, v139, v163
	v_min_f32_e32 v146, v137, v138
	v_max_f32_e32 v137, v137, v138
	s_waitcnt lgkmcnt(9)
	v_max_f32_e32 v136, v136, v136
	v_min_f32_e32 v173, v144, v172
	v_max_f32_e32 v145, v145, v145
	v_max_f32_e32 v144, v144, v172
	v_min_f32_e32 v171, v143, v170
	v_max_f32_e32 v143, v143, v170
	v_min_f32_e32 v169, v142, v168
	v_max_f32_e32 v142, v142, v168
	v_min_f32_e32 v167, v141, v166
	v_max_f32_e32 v141, v141, v166
	v_min_f32_e32 v165, v140, v164
	v_max_f32_e32 v140, v140, v164
	v_min_f32_e32 v163, v139, v146
	v_max_f32_e32 v139, v139, v146
	v_min_f32_e32 v138, v137, v136
	v_max_f32_e32 v136, v137, v136
	s_waitcnt lgkmcnt(8)
; #define INS16(A_, X_) do { float x_ = (X_); _Pragma("unroll") for (int i_ = 0; i_ < 16; ++i_) { const float hi_ = fmaxf(A_[i_], x_); x_ = fminf(A_[i_], x_); A_[i_] = hi_; } } while (0)
; __device__ __forceinline__ void p11_route(Frame& F) {
;     ...
;             for (int i = 0; i < 16; ++i) o[i] = __builtin_bit_cast(float, __builtin_amdgcn_ds_bpermute(((F.lane + 32) & 63) << 2, __builtin_bit_cast(int, a[i])));
; #pragma unroll
;             for (int i = 0; i < 16; ++i) INS16(a, o[i]);
	v_max_f32_e32 v135, v135, v135
	v_min_f32_e32 v174, v145, v173
	v_max_f32_e32 v147, v147, v147
	v_max_f32_e32 v145, v145, v173
	v_min_f32_e32 v172, v144, v171
	v_max_f32_e32 v144, v144, v171
	v_min_f32_e32 v170, v143, v169
	v_max_f32_e32 v143, v143, v169
	v_min_f32_e32 v168, v142, v167
	v_max_f32_e32 v142, v142, v167
	v_min_f32_e32 v166, v141, v165
	v_max_f32_e32 v141, v141, v165
	v_min_f32_e32 v164, v140, v163
	v_max_f32_e32 v140, v140, v163
	v_min_f32_e32 v146, v139, v138
	v_max_f32_e32 v138, v139, v138
	v_min_f32_e32 v137, v136, v135
	v_max_f32_e32 v135, v136, v135
	s_waitcnt lgkmcnt(7)
	v_max_f32_e32 v134, v134, v134
	v_min_f32_e32 v175, v147, v174
	v_max_f32_e32 v148, v148, v148
	v_max_f32_e32 v147, v147, v174
	v_min_f32_e32 v173, v145, v172
	v_max_f32_e32 v145, v145, v172
	v_min_f32_e32 v171, v144, v170
	v_max_f32_e32 v144, v144, v170
	v_min_f32_e32 v169, v143, v168
	v_max_f32_e32 v143, v143, v168
	v_min_f32_e32 v167, v142, v166
	v_max_f32_e32 v142, v142, v166
	v_min_f32_e32 v165, v141, v164
	v_max_f32_e32 v141, v141, v164
	v_min_f32_e32 v163, v140, v146
	v_max_f32_e32 v140, v140, v146
	v_min_f32_e32 v139, v138, v137
	v_max_f32_e32 v137, v138, v137
	v_min_f32_e32 v136, v135, v134
	v_max_f32_e32 v134, v135, v134
	s_waitcnt lgkmcnt(6)
	v_max_f32_e32 v133, v133, v133
	v_min_f32_e32 v176, v148, v175
	v_max_f32_e32 v149, v149, v149
	v_max_f32_e32 v148, v148, v175
	v_min_f32_e32 v174, v147, v173
	v_max_f32_e32 v147, v147, v173
	v_min_f32_e32 v172, v145, v171
	v_max_f32_e32 v145, v145, v171
	v_min_f32_e32 v170, v144, v169
	v_max_f32_e32 v144, v144, v169
	v_min_f32_e32 v168, v143, v167
	v_max_f32_e32 v143, v143, v167
	v_min_f32_e32 v166, v142, v165
	v_max_f32_e32 v142, v142, v165
	v_min_f32_e32 v164, v141, v163
	v_max_f32_e32 v141, v141, v163
	v_min_f32_e32 v146, v140, v139
	v_max_f32_e32 v139, v140, v139
	v_min_f32_e32 v138, v137, v136
	v_max_f32_e32 v136, v137, v136
	v_min_f32_e32 v135, v134, v133
	v_max_f32_e32 v133, v134, v133
	s_waitcnt lgkmcnt(5)
	v_max_f32_e32 v132, v132, v132
	v_min_f32_e32 v177, v149, v176
	v_max_f32_e32 v159, v159, v159
	v_max_f32_e32 v149, v149, v176
	v_min_f32_e32 v175, v148, v174
	v_max_f32_e32 v148, v148, v174
	v_min_f32_e32 v173, v147, v172
	v_max_f32_e32 v147, v147, v172
	v_min_f32_e32 v171, v145, v170
	v_max_f32_e32 v145, v145, v170
	v_min_f32_e32 v169, v144, v168
	v_max_f32_e32 v144, v144, v168
	v_min_f32_e32 v167, v143, v166
	v_max_f32_e32 v143, v143, v166
	v_min_f32_e32 v165, v142, v164
	v_max_f32_e32 v142, v142, v164
	v_min_f32_e32 v163, v141, v146
	v_max_f32_e32 v141, v141, v146
	v_min_f32_e32 v140, v139, v138
	v_max_f32_e32 v138, v139, v138
	v_min_f32_e32 v137, v136, v135
	v_max_f32_e32 v135, v136, v135
	v_min_f32_e32 v134, v133, v132
	v_max_f32_e32 v132, v133, v132
	s_waitcnt lgkmcnt(4)
	v_max_f32_e32 v131, v131, v131
	v_min_f32_e32 v178, v159, v177
	v_max_f32_e32 v161, v161, v161
	v_max_f32_e32 v159, v159, v177
	v_min_f32_e32 v176, v149, v175
	v_max_f32_e32 v149, v149, v175
	v_min_f32_e32 v174, v148, v173
	v_max_f32_e32 v148, v148, v173
	v_min_f32_e32 v172, v147, v171
	v_max_f32_e32 v147, v147, v171
	v_min_f32_e32 v170, v145, v169
	v_max_f32_e32 v145, v145, v169
	v_min_f32_e32 v168, v144, v167
	v_max_f32_e32 v144, v144, v167
	v_min_f32_e32 v166, v143, v165
	v_max_f32_e32 v143, v143, v165
	v_min_f32_e32 v164, v142, v163
	v_max_f32_e32 v142, v142, v163
	v_min_f32_e32 v146, v141, v140
	v_max_f32_e32 v140, v141, v140
	v_min_f32_e32 v139, v138, v137
	v_max_f32_e32 v137, v138, v137
	v_min_f32_e32 v136, v135, v134
	v_max_f32_e32 v134, v135, v134
	v_min_f32_e32 v133, v132, v131
	v_max_f32_e32 v131, v132, v131
	s_waitcnt lgkmcnt(3)
	v_max_f32_e32 v130, v130, v130
	v_min_f32_e32 v179, v161, v178
	v_max_f32_e32 v162, v162, v162
	v_max_f32_e32 v161, v161, v178
	v_min_f32_e32 v177, v159, v176
	v_max_f32_e32 v159, v159, v176
	v_min_f32_e32 v175, v149, v174
	v_max_f32_e32 v149, v149, v174
	v_min_f32_e32 v173, v148, v172
	v_max_f32_e32 v148, v148, v172
	v_min_f32_e32 v171, v147, v170
	v_max_f32_e32 v147, v147, v170
	v_min_f32_e32 v169, v145, v168
	v_max_f32_e32 v145, v145, v168
	v_min_f32_e32 v167, v144, v166
	v_max_f32_e32 v144, v144, v166
	v_min_f32_e32 v165, v143, v164
	v_max_f32_e32 v143, v143, v164
	v_min_f32_e32 v163, v142, v146
	v_max_f32_e32 v142, v142, v146
	v_min_f32_e32 v141, v140, v139
	v_max_f32_e32 v139, v140, v139
	v_min_f32_e32 v138, v137, v136
	v_max_f32_e32 v136, v137, v136
	v_min_f32_e32 v135, v134, v133
	v_max_f32_e32 v133, v134, v133
	v_min_f32_e32 v132, v131, v130
	v_max_f32_e32 v130, v131, v130
	s_waitcnt lgkmcnt(2)
	v_max_f32_e32 v128, v128, v128
	v_min_f32_e32 v180, v162, v179
	v_max_f32_e32 v160, v160, v160
	v_max_f32_e32 v162, v162, v179
	v_min_f32_e32 v178, v161, v177
	v_max_f32_e32 v161, v161, v177
	v_min_f32_e32 v176, v159, v175
	v_max_f32_e32 v159, v159, v175
	v_min_f32_e32 v174, v149, v173
	v_max_f32_e32 v149, v149, v173
	v_min_f32_e32 v172, v148, v171
	v_max_f32_e32 v148, v148, v171
	v_min_f32_e32 v170, v147, v169
	v_max_f32_e32 v147, v147, v169
	v_min_f32_e32 v168, v145, v167
	v_max_f32_e32 v145, v145, v167
	v_min_f32_e32 v166, v144, v165
	v_max_f32_e32 v144, v144, v165
	v_min_f32_e32 v164, v143, v163
	v_max_f32_e32 v143, v143, v163
	v_min_f32_e32 v146, v142, v141
	v_max_f32_e32 v141, v142, v141
	v_min_f32_e32 v140, v139, v138
	v_max_f32_e32 v138, v139, v138
	v_min_f32_e32 v137, v136, v135
	v_max_f32_e32 v135, v136, v135
	v_min_f32_e32 v134, v133, v132
	v_max_f32_e32 v132, v133, v132
	v_min_f32_e32 v131, v130, v128
	v_max_f32_e32 v128, v130, v128
	s_waitcnt lgkmcnt(1)
; #define INS16(A_, X_) do { float x_ = (X_); _Pragma("unroll") for (int i_ = 0; i_ < 16; ++i_) { const float hi_ = fmaxf(A_[i_], x_); x_ = fminf(A_[i_], x_); A_[i_] = hi_; } } while (0)
; __device__ __forceinline__ void p11_route(Frame& F) {
;     ...
;             for (int i = 0; i < 16; ++i) o[i] = __builtin_bit_cast(float, __builtin_amdgcn_ds_bpermute(((F.lane + 32) & 63) << 2, __builtin_bit_cast(int, a[i])));
; #pragma unroll
;             for (int i = 0; i < 16; ++i) INS16(a, o[i]);
	v_max_f32_e32 v127, v127, v127
	v_min_f32_e32 v181, v160, v180
	v_max_f32_e32 v160, v160, v180
	v_min_f32_e32 v179, v162, v178
	v_max_f32_e32 v162, v162, v178
	v_min_f32_e32 v177, v161, v176
	v_max_f32_e32 v161, v161, v176
	v_min_f32_e32 v175, v159, v174
	v_max_f32_e32 v159, v159, v174
	v_min_f32_e32 v173, v149, v172
	v_max_f32_e32 v149, v149, v172
	v_min_f32_e32 v171, v148, v170
	v_max_f32_e32 v148, v148, v170
	v_min_f32_e32 v169, v147, v168
	v_max_f32_e32 v147, v147, v168
	v_min_f32_e32 v167, v145, v166
	v_max_f32_e32 v145, v145, v166
	v_min_f32_e32 v165, v144, v164
	v_max_f32_e32 v144, v144, v164
	v_min_f32_e32 v163, v143, v146
	v_max_f32_e32 v143, v143, v146
	v_min_f32_e32 v142, v141, v140
	v_max_f32_e32 v140, v141, v140
	v_min_f32_e32 v139, v138, v137
	v_max_f32_e32 v137, v138, v137
	v_min_f32_e32 v136, v135, v134
	v_max_f32_e32 v134, v135, v134
	v_min_f32_e32 v133, v132, v131
	v_max_f32_e32 v131, v132, v131
	v_min_f32_e32 v130, v128, v127
	v_max_f32_e32 v127, v128, v127
	s_waitcnt lgkmcnt(0)
	v_max_f32_e32 v126, v126, v126
	v_min_f32_e32 v180, v160, v179
	v_max_f32_e32 v160, v160, v179
	v_min_f32_e32 v178, v162, v177
	v_max_f32_e32 v162, v162, v177
	v_min_f32_e32 v176, v161, v175
	v_max_f32_e32 v161, v161, v175
	v_min_f32_e32 v174, v159, v173
	v_max_f32_e32 v159, v159, v173
	v_min_f32_e32 v172, v149, v171
	v_max_f32_e32 v149, v149, v171
	v_min_f32_e32 v170, v148, v169
	v_max_f32_e32 v148, v148, v169
	v_min_f32_e32 v168, v147, v167
	v_max_f32_e32 v147, v147, v167
	v_min_f32_e32 v166, v145, v165
	v_max_f32_e32 v145, v145, v165
	v_min_f32_e32 v164, v144, v163
	v_max_f32_e32 v144, v144, v163
	v_min_f32_e32 v146, v143, v142
	v_max_f32_e32 v142, v143, v142
	v_min_f32_e32 v141, v140, v139
	v_max_f32_e32 v139, v140, v139
	v_min_f32_e32 v138, v137, v136
	v_max_f32_e32 v136, v137, v136
	v_min_f32_e32 v135, v134, v133
	v_max_f32_e32 v133, v134, v133
	v_min_f32_e32 v132, v131, v130
	v_max_f32_e32 v130, v131, v130
	v_min_f32_e32 v128, v127, v126
	v_min_f32_e32 v179, v160, v178
	v_max_f32_e32 v160, v160, v178
	v_min_f32_e32 v177, v162, v176
	v_max_f32_e32 v162, v162, v176
	v_min_f32_e32 v175, v161, v174
	v_max_f32_e32 v161, v161, v174
	v_min_f32_e32 v173, v159, v172
	v_max_f32_e32 v159, v159, v172
	v_min_f32_e32 v171, v149, v170
	v_max_f32_e32 v149, v149, v170
	v_min_f32_e32 v169, v148, v168
	v_max_f32_e32 v148, v148, v168
	v_min_f32_e32 v167, v147, v166
	v_max_f32_e32 v147, v147, v166
	v_min_f32_e32 v165, v145, v164
	v_max_f32_e32 v145, v145, v164
	v_min_f32_e32 v163, v144, v146
	v_max_f32_e32 v144, v144, v146
	v_min_f32_e32 v143, v142, v141
	v_max_f32_e32 v141, v142, v141
	v_min_f32_e32 v140, v139, v138
	v_max_f32_e32 v138, v139, v138
	v_min_f32_e32 v137, v136, v135
	v_max_f32_e32 v135, v136, v135
	v_min_f32_e32 v134, v133, v132
	v_max_f32_e32 v132, v133, v132
	v_min_f32_e32 v131, v130, v128
	v_min_f32_e32 v178, v160, v177
	v_max_f32_e32 v160, v160, v177
	v_min_f32_e32 v176, v162, v175
	v_max_f32_e32 v162, v162, v175
	v_min_f32_e32 v174, v161, v173
	v_max_f32_e32 v161, v161, v173
	v_min_f32_e32 v172, v159, v171
	v_max_f32_e32 v159, v159, v171
	v_min_f32_e32 v170, v149, v169
	v_max_f32_e32 v149, v149, v169
	v_min_f32_e32 v168, v148, v167
	v_max_f32_e32 v148, v148, v167
	v_min_f32_e32 v166, v147, v165
	v_max_f32_e32 v147, v147, v165
	v_min_f32_e32 v164, v145, v163
	v_max_f32_e32 v145, v145, v163
	v_min_f32_e32 v146, v144, v143
	v_max_f32_e32 v143, v144, v143
	v_min_f32_e32 v142, v141, v140
	v_max_f32_e32 v140, v141, v140
	v_min_f32_e32 v139, v138, v137
	v_max_f32_e32 v137, v138, v137
	v_min_f32_e32 v136, v135, v134
	v_max_f32_e32 v134, v135, v134
	v_min_f32_e32 v133, v132, v131
	v_min_f32_e32 v177, v160, v176
	v_max_f32_e32 v160, v160, v176
	v_min_f32_e32 v175, v162, v174
	v_max_f32_e32 v162, v162, v174
	v_min_f32_e32 v173, v161, v172
	v_max_f32_e32 v161, v161, v172
	v_min_f32_e32 v171, v159, v170
	v_max_f32_e32 v159, v159, v170
	v_min_f32_e32 v169, v149, v168
	v_max_f32_e32 v149, v149, v168
	v_min_f32_e32 v167, v148, v166
	v_max_f32_e32 v148, v148, v166
	v_min_f32_e32 v165, v147, v164
	v_max_f32_e32 v147, v147, v164
	v_min_f32_e32 v163, v145, v146
	v_max_f32_e32 v145, v145, v146
	v_min_f32_e32 v144, v143, v142
	v_max_f32_e32 v142, v143, v142
	v_min_f32_e32 v141, v140, v139
	v_max_f32_e32 v139, v140, v139
	v_min_f32_e32 v138, v137, v136
	v_max_f32_e32 v136, v137, v136
	v_min_f32_e32 v135, v134, v133
	v_min_f32_e32 v176, v160, v175
	v_max_f32_e32 v160, v160, v175
	v_min_f32_e32 v174, v162, v173
	v_max_f32_e32 v162, v162, v173
	v_min_f32_e32 v172, v161, v171
	v_max_f32_e32 v161, v161, v171
	v_min_f32_e32 v170, v159, v169
	v_max_f32_e32 v159, v159, v169
	v_min_f32_e32 v168, v149, v167
	v_max_f32_e32 v149, v149, v167
	v_min_f32_e32 v166, v148, v165
	v_max_f32_e32 v148, v148, v165
	v_min_f32_e32 v164, v147, v163
	v_max_f32_e32 v147, v147, v163
	v_min_f32_e32 v146, v145, v144
	v_max_f32_e32 v144, v145, v144
	v_min_f32_e32 v143, v142, v141
	v_max_f32_e32 v141, v142, v141
	v_min_f32_e32 v140, v139, v138
	v_max_f32_e32 v138, v139, v138
	v_min_f32_e32 v137, v136, v135
	v_min_f32_e32 v175, v160, v174
	v_max_f32_e32 v160, v160, v174
	v_min_f32_e32 v173, v162, v172
	v_max_f32_e32 v162, v162, v172
	v_min_f32_e32 v171, v161, v170
	v_max_f32_e32 v161, v161, v170
	v_min_f32_e32 v169, v159, v168
	v_max_f32_e32 v159, v159, v168
	v_min_f32_e32 v167, v149, v166
	v_max_f32_e32 v149, v149, v166
	v_min_f32_e32 v165, v148, v164
	v_max_f32_e32 v148, v148, v164
	v_min_f32_e32 v163, v147, v146
	v_max_f32_e32 v146, v147, v146
	v_min_f32_e32 v145, v144, v143
	v_max_f32_e32 v143, v144, v143
	v_min_f32_e32 v142, v141, v140
	v_max_f32_e32 v140, v141, v140
	v_min_f32_e32 v139, v138, v137
; #define INS16(A_, X_) do { float x_ = (X_); _Pragma("unroll") for (int i_ = 0; i_ < 16; ++i_) { const float hi_ = fmaxf(A_[i_], x_); x_ = fminf(A_[i_], x_); A_[i_] = hi_; } } while (0)
; __device__ __forceinline__ void p11_route(Frame& F) {
;     ...
;             for (int i = 0; i < 16; ++i) INS16(a, o[i]);
;           if (F.lane < 32) {
;             float tv[16]; int ti[16];
; #pragma unroll
;             for (int i = 0; i < 16; ++i) { ti[i] = 255 - (int)(__float_as_uint(a[i]) & 255u); tv[i] = row[ti[i]]; }
; #pragma unroll
;             for (int i = 0; i < 16; ++i) { row[i] = tv[i]; row[16 + i] = __int_as_float(ti[i]); }
;           } }
	v_min_f32_e32 v174, v160, v173
	v_max_f32_e32 v160, v160, v173
	v_min_f32_e32 v172, v162, v171
	v_max_f32_e32 v162, v162, v171
	v_min_f32_e32 v170, v161, v169
	v_max_f32_e32 v161, v161, v169
	v_min_f32_e32 v168, v159, v167
	v_max_f32_e32 v159, v159, v167
	v_min_f32_e32 v166, v149, v165
	v_max_f32_e32 v149, v149, v165
	v_min_f32_e32 v164, v148, v163
	v_max_f32_e32 v148, v148, v163
	v_min_f32_e32 v147, v146, v145
	v_max_f32_e32 v145, v146, v145
	v_min_f32_e32 v144, v143, v142
	v_max_f32_e32 v142, v143, v142
	v_min_f32_e32 v141, v140, v139
	v_min_f32_e32 v173, v160, v172
	v_max_f32_e32 v160, v160, v172
	v_min_f32_e32 v171, v162, v170
	v_max_f32_e32 v162, v162, v170
	v_min_f32_e32 v169, v161, v168
	v_max_f32_e32 v161, v161, v168
	v_min_f32_e32 v167, v159, v166
	v_max_f32_e32 v159, v159, v166
	v_min_f32_e32 v165, v149, v164
	v_max_f32_e32 v149, v149, v164
	v_min_f32_e32 v163, v148, v147
	v_max_f32_e32 v147, v148, v147
	v_min_f32_e32 v146, v145, v144
	v_max_f32_e32 v144, v145, v144
	v_min_f32_e32 v143, v142, v141
	v_max3_f32 v129, v129, v181, v180
	v_min_f32_e32 v172, v160, v171
	v_max_f32_e32 v160, v160, v171
	v_min_f32_e32 v170, v162, v169
	v_max_f32_e32 v162, v162, v169
	v_min_f32_e32 v168, v161, v167
	v_max_f32_e32 v161, v161, v167
	v_min_f32_e32 v166, v159, v165
	v_max_f32_e32 v159, v159, v165
	v_min_f32_e32 v164, v149, v163
	v_max_f32_e32 v149, v149, v163
	v_min_f32_e32 v148, v147, v146
	v_max_f32_e32 v146, v147, v146
	v_min_f32_e32 v145, v144, v143
	v_max3_f32 v129, v129, v179, v178
	v_min_f32_e32 v171, v160, v170
	v_max_f32_e32 v160, v160, v170
	v_min_f32_e32 v169, v162, v168
	v_max_f32_e32 v162, v162, v168
	v_min_f32_e32 v167, v161, v166
	v_max_f32_e32 v161, v161, v166
	v_min_f32_e32 v165, v159, v164
	v_max_f32_e32 v159, v159, v164
	v_min_f32_e32 v163, v149, v148
	v_max_f32_e32 v148, v149, v148
	v_min_f32_e32 v147, v146, v145
	v_max3_f32 v129, v129, v177, v176
	v_min_f32_e32 v170, v160, v169
	v_max_f32_e32 v160, v160, v169
	v_min_f32_e32 v168, v162, v167
	v_max_f32_e32 v162, v162, v167
	v_min_f32_e32 v166, v161, v165
	v_max_f32_e32 v161, v161, v165
	v_min_f32_e32 v164, v159, v163
	v_max_f32_e32 v159, v159, v163
	v_min_f32_e32 v149, v148, v147
	v_max3_f32 v129, v129, v175, v174
	v_min_f32_e32 v169, v160, v168
	v_max_f32_e32 v160, v160, v168
	v_min_f32_e32 v167, v162, v166
	v_max_f32_e32 v162, v162, v166
	v_min_f32_e32 v165, v161, v164
	v_max_f32_e32 v161, v161, v164
	v_min_f32_e32 v163, v159, v149
	v_max3_f32 v129, v129, v173, v172
	v_min_f32_e32 v168, v160, v167
	v_max_f32_e32 v160, v160, v167
	v_min_f32_e32 v166, v162, v165
	v_max_f32_e32 v162, v162, v165
	v_min_f32_e32 v164, v161, v163
	v_max3_f32 v129, v129, v171, v170
	v_min_f32_e32 v167, v160, v166
	v_max_f32_e32 v160, v160, v166
	v_min_f32_e32 v165, v162, v164
	v_max3_f32 v129, v129, v169, v168
	v_min_f32_e32 v166, v160, v165
	v_max3_f32 v129, v129, v167, v166
	v_max_f32_e32 v126, v127, v126
	v_max_f32_e32 v127, v130, v128
	v_max_f32_e32 v128, v132, v131
	v_max_f32_e32 v130, v134, v133
	v_max_f32_e32 v131, v136, v135
	v_max_f32_e32 v132, v138, v137
	v_max_f32_e32 v133, v140, v139
	v_max_f32_e32 v134, v142, v141
	v_max_f32_e32 v135, v144, v143
	v_max_f32_e32 v136, v146, v145
	v_max_f32_e32 v137, v148, v147
	v_max_f32_e32 v138, v159, v149
	v_max_f32_e32 v139, v161, v163
	v_max_f32_e32 v140, v162, v164
	v_max_f32_e32 v141, v160, v165
	v_xor_b32_e32 v127, -1, v127
	v_xor_b32_e32 v126, -1, v126
	v_xor_b32_e32 v130, -1, v130
	v_xor_b32_e32 v128, -1, v128
	v_xor_b32_e32 v132, -1, v132
	v_xor_b32_e32 v131, -1, v131
	v_xor_b32_e32 v134, -1, v134
	v_xor_b32_e32 v133, -1, v133
	v_xor_b32_e32 v136, -1, v136
	v_xor_b32_e32 v135, -1, v135
	v_xor_b32_e32 v138, -1, v138
	v_xor_b32_e32 v137, -1, v137
	v_xor_b32_e32 v140, -1, v140
	v_xor_b32_e32 v139, -1, v139
	v_xor_b32_e32 v129, -1, v129
	v_xor_b32_e32 v141, -1, v141
	v_and_b32_e32 v127, 0xff, v127
	v_and_b32_e32 v126, 0xff, v126
	v_and_b32_e32 v130, 0xff, v130
	v_and_b32_e32 v128, 0xff, v128
	v_and_b32_e32 v132, 0xff, v132
	v_and_b32_e32 v131, 0xff, v131
	v_and_b32_e32 v134, 0xff, v134
	v_and_b32_e32 v133, 0xff, v133
	v_and_b32_e32 v136, 0xff, v136
	v_and_b32_e32 v135, 0xff, v135
	v_and_b32_e32 v138, 0xff, v138
	v_and_b32_e32 v137, 0xff, v137
	v_and_b32_e32 v140, 0xff, v140
	v_and_b32_e32 v139, 0xff, v139
	v_and_b32_e32 v129, 0xff, v129
	v_and_b32_e32 v141, 0xff, v141
	v_lshl_add_u32 v142, v126, 2, v152
	v_lshl_add_u32 v143, v127, 2, v152
	v_lshl_add_u32 v144, v128, 2, v152
	v_lshl_add_u32 v145, v130, 2, v152
	v_lshl_add_u32 v146, v131, 2, v152
	v_lshl_add_u32 v147, v132, 2, v152
	v_lshl_add_u32 v148, v133, 2, v152
	v_lshl_add_u32 v149, v134, 2, v152
	v_lshl_add_u32 v159, v135, 2, v152
	v_lshl_add_u32 v160, v136, 2, v152
	v_lshl_add_u32 v161, v137, 2, v152
	v_lshl_add_u32 v162, v138, 2, v152
	v_lshl_add_u32 v163, v139, 2, v152
	v_lshl_add_u32 v164, v140, 2, v152
	v_lshl_add_u32 v165, v141, 2, v152
	v_lshl_add_u32 v166, v129, 2, v152
	ds_read_b32 v142, v142
	ds_read_b32 v143, v143
	ds_read_b32 v144, v144
	ds_read_b32 v145, v145
	ds_read_b32 v146, v146
	ds_read_b32 v147, v147
	ds_read_b32 v148, v148
	ds_read_b32 v149, v149
	ds_read_b32 v159, v159
	ds_read_b32 v160, v160
	ds_read_b32 v161, v161
	ds_read_b32 v162, v162
	ds_read_b32 v163, v163
	ds_read_b32 v164, v164
	ds_read_b32 v165, v165
	ds_read_b32 v166, v166
	s_waitcnt lgkmcnt(14)
	ds_write2_b32 v152, v142, v143 offset1:1
	ds_write2_b32 v152, v126, v127 offset0:16 offset1:17
	s_waitcnt lgkmcnt(14)
	ds_write2_b32 v152, v144, v145 offset0:2 offset1:3
	ds_write2_b32 v152, v128, v130 offset0:18 offset1:19
	s_waitcnt lgkmcnt(14)
	ds_write2_b32 v152, v146, v147 offset0:4 offset1:5
	ds_write2_b32 v152, v131, v132 offset0:20 offset1:21
	s_waitcnt lgkmcnt(14)
	ds_write2_b32 v152, v148, v149 offset0:6 offset1:7
	ds_write2_b32 v152, v133, v134 offset0:22 offset1:23
	s_waitcnt lgkmcnt(14)
	ds_write2_b32 v152, v159, v160 offset0:8 offset1:9
	ds_write2_b32 v152, v135, v136 offset0:24 offset1:25
	s_waitcnt lgkmcnt(14)
	ds_write2_b32 v152, v161, v162 offset0:10 offset1:11
	ds_write2_b32 v152, v137, v138 offset0:26 offset1:27
	s_waitcnt lgkmcnt(14)
	ds_write2_b32 v152, v163, v164 offset0:12 offset1:13
	ds_write2_b32 v152, v139, v140 offset0:28 offset1:29
	s_waitcnt lgkmcnt(14)
	ds_write2_b32 v152, v165, v166 offset0:14 offset1:15
	ds_write2_b32 v152, v141, v129 offset0:30 offset1:31
	s_or_b64 exec, exec, s[4:5]
	s_and_saveexec_b64 s[12:13], s[2:3]
	s_cbranch_execz .LBB0_3213
	s_branch .LBB0_3219
